# code placement: every MFMA of the five GEMM K-loops on an 8-byte boundary (one s_nop 0 pad at the head of a load segment where needed, loop length kept even)
# speedup vs baseline: 1.0146x; 1.0146x over previous
; #define PG8_STAGE(bufoff, gbase, voff) do { _Pragma("unroll") for (int _i = 0; _i < 2; ++_i) \
;         __builtin_amdgcn_global_load_lds((const unsigned*)((const char*)(gbase) + (voff)[_i]), (PG8_LAS unsigned*)(lds + (bufoff) + ldsw + _i * 8192), 16, 0, 0); } while (0)
; #define PG8_LDA(dst, b, h) do { _Pragma("unroll") for (int m = 0; m < 4; ++m) _Pragma("unroll") for (int k = 0; k < 2; ++k) dst[m][k] = *(const PG8_LAS bf16x8*)(lds + PG8_SA(b, h) + aoff + m * 2048 + k * 1024); } while (0)
; #define PG8_LDB(dst, b, h) do { _Pragma("unroll") for (int n = 0; n < 2; ++n) _Pragma("unroll") for (int k = 0; k < 2; ++k) dst[n][k] = *(const PG8_LAS bf16x8*)(lds + PG8_SB(b, h) + boff + n * 2048 + k * 1024); } while (0)
; template <class Epi, class Sched, bool ALIGN_EPI = false, bool SP2 = false>
; __device__ __forceinline__ void gemm_phase(PG8_LAS unsigned char* lds, const Gemm g, const Sched& S, const Epi& E) {
;     ...
;         for (; t < tend; t += 2) {
;             const bool last = (t == nt - 2);
;             const char* a1 = cA + (size_t)(t + 1) * kstep;
;             const char* a2 = last ? nA : cA + (size_t)(t + 2) * kstep; const char* b2 = last ? nB : cB + (size_t)(t + 2) * kstep;
;             const char* a3 = a2 + kstep; const char* b3 = b2 + kstep;
;             if (last && has_next) S.a_ready(nxt);
;             if constexpr (SP2) {
;             PG8_LDB(B0, 0, 0); PG8_LDB(B1, 0, 1); PG8_SCHED; PG8_LDA(At, 0, 0); PG8_STAGEA(PG8_SA(1, 1), a1, 1, false);
;             PG8_WAIT_V(8); PG8_WAIT_L(0); PG8_BAR; PG8_MMA(0, 0, At, B0); PG8_MMA(0, 1, At, B1); PG8_BAR; PG8_SCHED;
;             PG8_LDA(At, 0, 1); PG8_STAGE(PG8_SB(0, 0), b2, voffB); PG8_STAGE(PG8_SB(0, 1), b2 + hstep, voffB); PG8_STAGEA(PG8_SA(0, 0), a2, 0, last);
;             PG8_WAIT_V(8); PG8_WAIT_L(0); PG8_BAR; PG8_MMA(1, 0, At, B0); PG8_MMA(1, 1, At, B1); PG8_BAR; PG8_SCHED;
;             PG8_LDB(B0, 1, 0); PG8_LDB(B1, 1, 1); PG8_SCHED; PG8_LDA(At, 1, 0); PG8_STAGEA(PG8_SA(0, 1), a2, 1, last);
;             PG8_WAIT_V(8); PG8_WAIT_L(0); PG8_BAR; PG8_MMA(0, 0, At, B0); PG8_MMA(0, 1, At, B1); PG8_BAR; PG8_SCHED;
;             PG8_LDA(At, 1, 1); PG8_STAGE(PG8_SB(1, 0), b3, voffB); PG8_STAGE(PG8_SB(1, 1), b3 + hstep, voffB); PG8_STAGEA(PG8_SA(1, 0), a3, 0, last);
;             PG8_WAIT_V(8); PG8_WAIT_L(0); PG8_BAR; PG8_MMA(1, 0, At, B0); PG8_MMA(1, 1, At, B1); PG8_BAR; PG8_SCHED;
.LBB0_110:
	v_add_u32_e32 v142, s79, v170
	v_add_u32_e32 v175, s80, v170
	ds_read_b128 v[130:133], v142
	ds_read_b128 v[134:137], v142 offset:1024
	ds_read_b128 v[138:141], v142 offset:2048
	ds_read_b128 v[142:145], v142 offset:3072
	ds_read_b128 v[162:165], v175
	ds_read_b128 v[166:169], v175 offset:1024
	ds_read_b128 v[176:179], v175 offset:2048
	ds_read_b128 v[180:183], v175 offset:3072
	s_add_u32 s54, s10, 0xfff80080
	s_addc_u32 s55, s11, -1
	s_cmp_eq_u32 s49, 28
	s_cselect_b32 s61, s9, s55
	s_cselect_b32 s60, s18, s54
	s_cselect_b32 s55, s19, s47
	s_cselect_b32 s54, s36, s37
	v_lshl_add_u64 v[200:201], s[10:11], 0, v[154:155]
	s_add_i32 m0, s57, 0xc000
	ds_read_b128 v[184:187], v174
	ds_read_b128 v[188:191], v174 offset:1024
	ds_read_b128 v[192:195], v174 offset:2048
	ds_read_b128 v[196:199], v174 offset:3072
	ds_read_b128 v[204:207], v174 offset:4096
	ds_read_b128 v[208:211], v174 offset:5120
	ds_read_b128 v[212:215], v174 offset:6144
	ds_read_b128 v[216:219], v174 offset:7168
	global_load_lds_dwordx4 v[200:201], off
	v_lshl_add_u64 v[200:201], s[10:11], 0, v[156:157]
	s_add_i32 m0, s57, 0xe000
	s_nop 0
	global_load_lds_dwordx4 v[200:201], off
	s_waitcnt vmcnt(8) lgkmcnt(0)
	s_barrier
	s_setprio 1
	v_mfma_f32_16x16x32_bf16 v[114:117], v[130:133], v[184:187], v[114:117]
	v_mfma_f32_16x16x32_bf16 v[118:121], v[138:141], v[184:187], v[118:121]
	v_mfma_f32_16x16x32_bf16 v[98:101], v[130:133], v[192:195], v[98:101]
	v_mfma_f32_16x16x32_bf16 v[102:105], v[138:141], v[192:195], v[102:105]
	v_mfma_f32_16x16x32_bf16 v[82:85], v[130:133], v[204:207], v[82:85]
	v_mfma_f32_16x16x32_bf16 v[86:89], v[138:141], v[204:207], v[86:89]
	v_mfma_f32_16x16x32_bf16 v[66:69], v[130:133], v[212:215], v[66:69]
	v_mfma_f32_16x16x32_bf16 v[70:73], v[138:141], v[212:215], v[70:73]
	v_mfma_f32_16x16x32_bf16 v[114:117], v[134:137], v[188:191], v[114:117]
	v_mfma_f32_16x16x32_bf16 v[118:121], v[142:145], v[188:191], v[118:121]
	v_mfma_f32_16x16x32_bf16 v[98:101], v[134:137], v[196:199], v[98:101]
	v_mfma_f32_16x16x32_bf16 v[102:105], v[142:145], v[196:199], v[102:105]
	v_mfma_f32_16x16x32_bf16 v[82:85], v[134:137], v[208:211], v[82:85]
	v_mfma_f32_16x16x32_bf16 v[86:89], v[142:145], v[208:211], v[86:89]
	v_mfma_f32_16x16x32_bf16 v[66:69], v[134:137], v[216:219], v[66:69]
	v_mfma_f32_16x16x32_bf16 v[70:73], v[142:145], v[216:219], v[70:73]
	v_mfma_f32_16x16x32_bf16 v[122:125], v[162:165], v[184:187], v[122:125]
	v_mfma_f32_16x16x32_bf16 v[126:129], v[176:179], v[184:187], v[126:129]
	v_mfma_f32_16x16x32_bf16 v[106:109], v[162:165], v[192:195], v[106:109]
	v_mfma_f32_16x16x32_bf16 v[110:113], v[176:179], v[192:195], v[110:113]
	v_mfma_f32_16x16x32_bf16 v[90:93], v[162:165], v[204:207], v[90:93]
	v_mfma_f32_16x16x32_bf16 v[94:97], v[176:179], v[204:207], v[94:97]
	v_mfma_f32_16x16x32_bf16 v[74:77], v[162:165], v[212:215], v[74:77]
	v_mfma_f32_16x16x32_bf16 v[78:81], v[176:179], v[212:215], v[78:81]
	v_mfma_f32_16x16x32_bf16 v[122:125], v[166:169], v[188:191], v[122:125]
	v_mfma_f32_16x16x32_bf16 v[126:129], v[180:183], v[188:191], v[126:129]
	v_mfma_f32_16x16x32_bf16 v[106:109], v[166:169], v[196:199], v[106:109]
	v_mfma_f32_16x16x32_bf16 v[110:113], v[180:183], v[196:199], v[110:113]
	v_mfma_f32_16x16x32_bf16 v[90:93], v[166:169], v[208:211], v[90:93]
	v_mfma_f32_16x16x32_bf16 v[94:97], v[180:183], v[208:211], v[94:97]
	v_mfma_f32_16x16x32_bf16 v[74:77], v[166:169], v[216:219], v[74:77]
	v_mfma_f32_16x16x32_bf16 v[78:81], v[180:183], v[216:219], v[78:81]
	s_setprio 0
	s_barrier
	s_nop 0
	s_add_i32 s59, s79, s66
	v_lshl_add_u64 v[200:201], s[54:55], 0, v[148:149]
	s_mov_b32 m0, s59
	ds_read_b128 v[184:187], v174 offset:16384
	ds_read_b128 v[188:191], v174 offset:17408
	ds_read_b128 v[192:195], v174 offset:18432
	ds_read_b128 v[196:199], v174 offset:19456
	ds_read_b128 v[204:207], v174 offset:20480
	ds_read_b128 v[208:211], v174 offset:21504
	ds_read_b128 v[212:215], v174 offset:22528
	ds_read_b128 v[216:219], v174 offset:23552
	global_load_lds_dwordx4 v[200:201], off
	s_add_i32 m0, s59, 0x2000
	s_add_u32 s62, s54, 0x80000
	v_lshl_add_u64 v[220:221], s[54:55], 0, v[152:153]
	s_addc_u32 s63, s55, 0
	s_add_i32 s59, s80, s66
	global_load_lds_dwordx4 v[220:221], off
	v_lshl_add_u64 v[222:223], s[62:63], 0, v[148:149]
	s_mov_b32 m0, s59
	v_lshl_add_u64 v[224:225], s[60:61], 0, v[150:151]
	global_load_lds_dwordx4 v[222:223], off
	v_lshl_add_u64 v[222:223], s[62:63], 0, v[152:153]
	s_add_i32 m0, s59, 0x2000
	s_nop 0
	global_load_lds_dwordx4 v[222:223], off
	v_lshl_add_u64 v[222:223], s[60:61], 0, v[146:147]
	s_mov_b32 m0, s57
	s_nop 0
	global_load_lds_dwordx4 v[222:223], off
	s_mov_b32 m0, s67
	s_nop 0
	global_load_lds_dwordx4 v[224:225], off
	s_waitcnt vmcnt(8) lgkmcnt(0)
	s_barrier
; #define PG8_LDA(dst, b, h) do { _Pragma("unroll") for (int m = 0; m < 4; ++m) _Pragma("unroll") for (int k = 0; k < 2; ++k) dst[m][k] = *(const PG8_LAS bf16x8*)(lds + PG8_SA(b, h) + aoff + m * 2048 + k * 1024); } while (0)
; #define PG8_LDB(dst, b, h) do { _Pragma("unroll") for (int n = 0; n < 2; ++n) _Pragma("unroll") for (int k = 0; k < 2; ++k) dst[n][k] = *(const PG8_LAS bf16x8*)(lds + PG8_SB(b, h) + boff + n * 2048 + k * 1024); } while (0)
; #define PG8_MMA(ai, bj, At, Bt) do { __builtin_amdgcn_s_setprio(1); _Pragma("unroll") for (int m = 0; m < 4; ++m) _Pragma("unroll") for (int n = 0; n < 2; ++n) _Pragma("unroll") for (int k = 0; k < 2; ++k) \
;         acc[ai][bj][m][n] = __builtin_amdgcn_mfma_f32_16x16x32_bf16(Bt[n][k], At[m][k], acc[ai][bj][m][n], 0, 0, 0); __builtin_amdgcn_s_setprio(0); } while (0)
; #define PG8_WAIT_V(n) asm volatile("s_waitcnt vmcnt(" #n ")" ::: "memory")
; #define PG8_WAIT_L(n) asm volatile("s_waitcnt lgkmcnt(" #n ")" ::: "memory")
; #define PG8_BAR __builtin_amdgcn_s_barrier()
; #define PG8_SCHED __builtin_amdgcn_sched_barrier(0)
; template <class Epi, class Sched, bool ALIGN_EPI = false, bool SP2 = false>
; __device__ __forceinline__ void gemm_phase(PG8_LAS unsigned char* lds, const Gemm g, const Sched& S, const Epi& E) {
;     ...
;             PG8_WAIT_V(8); PG8_WAIT_L(0); PG8_BAR; PG8_MMA(1, 0, At, B0); PG8_MMA(1, 1, At, B1); PG8_BAR; PG8_SCHED;
;             PG8_LDB(B0, 1, 0); PG8_LDB(B1, 1, 1); PG8_SCHED; PG8_LDA(At, 1, 0); PG8_STAGEA(PG8_SA(0, 1), a2, 1, last);
;             PG8_WAIT_V(8); PG8_WAIT_L(0); PG8_BAR; PG8_MMA(0, 0, At, B0); PG8_MMA(0, 1, At, B1); PG8_BAR; PG8_SCHED;
	s_setprio 1
	v_mfma_f32_16x16x32_bf16 v[58:61], v[130:133], v[184:187], v[58:61]
	v_mfma_f32_16x16x32_bf16 v[62:65], v[138:141], v[184:187], v[62:65]
	v_mfma_f32_16x16x32_bf16 v[42:45], v[130:133], v[192:195], v[42:45]
	v_mfma_f32_16x16x32_bf16 v[46:49], v[138:141], v[192:195], v[46:49]
	v_mfma_f32_16x16x32_bf16 v[18:21], v[130:133], v[204:207], v[18:21]
	v_mfma_f32_16x16x32_bf16 v[22:25], v[138:141], v[204:207], v[22:25]
	v_mfma_f32_16x16x32_bf16 v[6:9], v[130:133], v[212:215], v[6:9]
	v_mfma_f32_16x16x32_bf16 v[14:17], v[138:141], v[212:215], v[14:17]
	v_mfma_f32_16x16x32_bf16 v[58:61], v[134:137], v[188:191], v[58:61]
	v_mfma_f32_16x16x32_bf16 v[62:65], v[142:145], v[188:191], v[62:65]
	v_mfma_f32_16x16x32_bf16 v[42:45], v[134:137], v[196:199], v[42:45]
	v_mfma_f32_16x16x32_bf16 v[46:49], v[142:145], v[196:199], v[46:49]
	v_mfma_f32_16x16x32_bf16 v[18:21], v[134:137], v[208:211], v[18:21]
	v_mfma_f32_16x16x32_bf16 v[22:25], v[142:145], v[208:211], v[22:25]
	v_mfma_f32_16x16x32_bf16 v[6:9], v[134:137], v[216:219], v[6:9]
	v_mfma_f32_16x16x32_bf16 v[14:17], v[142:145], v[216:219], v[14:17]
	v_mfma_f32_16x16x32_bf16 v[50:53], v[162:165], v[184:187], v[50:53]
	v_mfma_f32_16x16x32_bf16 v[54:57], v[176:179], v[184:187], v[54:57]
	v_mfma_f32_16x16x32_bf16 v[34:37], v[162:165], v[192:195], v[34:37]
	v_mfma_f32_16x16x32_bf16 v[38:41], v[176:179], v[192:195], v[38:41]
	v_mfma_f32_16x16x32_bf16 v[26:29], v[162:165], v[204:207], v[26:29]
	v_mfma_f32_16x16x32_bf16 v[30:33], v[176:179], v[204:207], v[30:33]
	v_mfma_f32_16x16x32_bf16 v[10:13], v[162:165], v[212:215], v[10:13]
	v_mfma_f32_16x16x32_bf16 v[2:5], v[176:179], v[212:215], v[2:5]
	v_mfma_f32_16x16x32_bf16 v[50:53], v[166:169], v[188:191], v[50:53]
	v_mfma_f32_16x16x32_bf16 v[54:57], v[180:183], v[188:191], v[54:57]
	v_mfma_f32_16x16x32_bf16 v[34:37], v[166:169], v[196:199], v[34:37]
	v_mfma_f32_16x16x32_bf16 v[38:41], v[180:183], v[196:199], v[38:41]
	v_mfma_f32_16x16x32_bf16 v[26:29], v[166:169], v[208:211], v[26:29]
	v_mfma_f32_16x16x32_bf16 v[30:33], v[180:183], v[208:211], v[30:33]
	v_mfma_f32_16x16x32_bf16 v[10:13], v[166:169], v[216:219], v[10:13]
	v_mfma_f32_16x16x32_bf16 v[2:5], v[180:183], v[216:219], v[2:5]
	s_setprio 0
	s_barrier
	s_nop 0
	s_add_i32 s59, 0, 0x18000
	s_add_i32 s62, 0, 0x1c000
	v_add_u32_e32 v142, s59, v170
	v_add_u32_e32 v175, s62, v170
	ds_read_b128 v[130:133], v142
	ds_read_b128 v[134:137], v142 offset:1024
	ds_read_b128 v[138:141], v142 offset:2048
	ds_read_b128 v[142:145], v142 offset:3072
	ds_read_b128 v[162:165], v175
	ds_read_b128 v[166:169], v175 offset:1024
	ds_read_b128 v[176:179], v175 offset:2048
	ds_read_b128 v[180:183], v175 offset:3072
	s_add_u32 s60, s60, 0x80000
	s_addc_u32 s61, s61, 0
	s_mov_b32 m0, s68
	v_lshl_add_u64 v[226:227], s[60:61], 0, v[146:147]
	ds_read_b128 v[184:187], v174 offset:32768
	ds_read_b128 v[188:191], v174 offset:33792
	ds_read_b128 v[192:195], v174 offset:34816
	ds_read_b128 v[196:199], v174 offset:35840
	ds_read_b128 v[204:207], v174 offset:36864
	ds_read_b128 v[208:211], v174 offset:37888
	ds_read_b128 v[212:215], v174 offset:38912
	ds_read_b128 v[216:219], v174 offset:39936
	global_load_lds_dwordx4 v[226:227], off
	v_lshl_add_u64 v[226:227], s[60:61], 0, v[150:151]
	s_mov_b32 m0, s69
	s_nop 0
	global_load_lds_dwordx4 v[226:227], off
	s_waitcnt vmcnt(8) lgkmcnt(0)
	s_barrier
	s_setprio 1
	v_mfma_f32_16x16x32_bf16 v[114:117], v[130:133], v[184:187], v[114:117]
	v_mfma_f32_16x16x32_bf16 v[118:121], v[138:141], v[184:187], v[118:121]
	v_mfma_f32_16x16x32_bf16 v[98:101], v[130:133], v[192:195], v[98:101]
	v_mfma_f32_16x16x32_bf16 v[102:105], v[138:141], v[192:195], v[102:105]
	v_mfma_f32_16x16x32_bf16 v[82:85], v[130:133], v[204:207], v[82:85]
	v_mfma_f32_16x16x32_bf16 v[86:89], v[138:141], v[204:207], v[86:89]
	v_mfma_f32_16x16x32_bf16 v[66:69], v[130:133], v[212:215], v[66:69]
	v_mfma_f32_16x16x32_bf16 v[70:73], v[138:141], v[212:215], v[70:73]
	v_mfma_f32_16x16x32_bf16 v[114:117], v[134:137], v[188:191], v[114:117]
	v_mfma_f32_16x16x32_bf16 v[118:121], v[142:145], v[188:191], v[118:121]
	v_mfma_f32_16x16x32_bf16 v[98:101], v[134:137], v[196:199], v[98:101]
	v_mfma_f32_16x16x32_bf16 v[102:105], v[142:145], v[196:199], v[102:105]
	v_mfma_f32_16x16x32_bf16 v[82:85], v[134:137], v[208:211], v[82:85]
	v_mfma_f32_16x16x32_bf16 v[86:89], v[142:145], v[208:211], v[86:89]
	v_mfma_f32_16x16x32_bf16 v[66:69], v[134:137], v[216:219], v[66:69]
	v_mfma_f32_16x16x32_bf16 v[70:73], v[142:145], v[216:219], v[70:73]
	v_mfma_f32_16x16x32_bf16 v[122:125], v[162:165], v[184:187], v[122:125]
	v_mfma_f32_16x16x32_bf16 v[126:129], v[176:179], v[184:187], v[126:129]
	v_mfma_f32_16x16x32_bf16 v[106:109], v[162:165], v[192:195], v[106:109]
	v_mfma_f32_16x16x32_bf16 v[110:113], v[176:179], v[192:195], v[110:113]
	v_mfma_f32_16x16x32_bf16 v[90:93], v[162:165], v[204:207], v[90:93]
	v_mfma_f32_16x16x32_bf16 v[94:97], v[176:179], v[204:207], v[94:97]
	v_mfma_f32_16x16x32_bf16 v[74:77], v[162:165], v[212:215], v[74:77]
	v_mfma_f32_16x16x32_bf16 v[78:81], v[176:179], v[212:215], v[78:81]
	v_mfma_f32_16x16x32_bf16 v[122:125], v[166:169], v[188:191], v[122:125]
	v_mfma_f32_16x16x32_bf16 v[126:129], v[180:183], v[188:191], v[126:129]
	v_mfma_f32_16x16x32_bf16 v[106:109], v[166:169], v[196:199], v[106:109]
	v_mfma_f32_16x16x32_bf16 v[110:113], v[180:183], v[196:199], v[110:113]
	v_mfma_f32_16x16x32_bf16 v[90:93], v[166:169], v[208:211], v[90:93]
	v_mfma_f32_16x16x32_bf16 v[94:97], v[180:183], v[208:211], v[94:97]
	v_mfma_f32_16x16x32_bf16 v[74:77], v[166:169], v[216:219], v[74:77]
	v_mfma_f32_16x16x32_bf16 v[78:81], v[180:183], v[216:219], v[78:81]
	s_setprio 0
	s_barrier
; #define PG8_STAGE(bufoff, gbase, voff) do { _Pragma("unroll") for (int _i = 0; _i < 2; ++_i) \
;         __builtin_amdgcn_global_load_lds((const unsigned*)((const char*)(gbase) + (voff)[_i]), (PG8_LAS unsigned*)(lds + (bufoff) + ldsw + _i * 8192), 16, 0, 0); } while (0)
; #define PG8_LDA(dst, b, h) do { _Pragma("unroll") for (int m = 0; m < 4; ++m) _Pragma("unroll") for (int k = 0; k < 2; ++k) dst[m][k] = *(const PG8_LAS bf16x8*)(lds + PG8_SA(b, h) + aoff + m * 2048 + k * 1024); } while (0)
; #define PG8_LDB(dst, b, h) do { _Pragma("unroll") for (int n = 0; n < 2; ++n) _Pragma("unroll") for (int k = 0; k < 2; ++k) dst[n][k] = *(const PG8_LAS bf16x8*)(lds + PG8_SB(b, h) + boff + n * 2048 + k * 1024); } while (0)
; template <class Epi, class Sched, bool ALIGN_EPI = false, bool SP2 = false>
; __device__ __forceinline__ void gemm_phase(PG8_LAS unsigned char* lds, const Gemm g, const Sched& S, const Epi& E) {
;     ...
;         for (; t < tend; t += 2) {
;             const bool last = (t == nt - 2);
;             const char* a1 = cA + (size_t)(t + 1) * kstep;
;             const char* a2 = last ? nA : cA + (size_t)(t + 2) * kstep; const char* b2 = last ? nB : cB + (size_t)(t + 2) * kstep;
;             const char* a3 = a2 + kstep; const char* b3 = b2 + kstep;
;             if (last && has_next) S.a_ready(nxt);
;             if constexpr (SP2) {
;             PG8_LDB(B0, 0, 0); PG8_LDB(B1, 0, 1); PG8_SCHED; PG8_LDA(At, 0, 0); PG8_STAGEA(PG8_SA(1, 1), a1, 1, false);
;             PG8_WAIT_V(8); PG8_WAIT_L(0); PG8_BAR; PG8_MMA(0, 0, At, B0); PG8_MMA(0, 1, At, B1); PG8_BAR; PG8_SCHED;
;             PG8_LDA(At, 0, 1); PG8_STAGE(PG8_SB(0, 0), b2, voffB); PG8_STAGE(PG8_SB(0, 1), b2 + hstep, voffB); PG8_STAGEA(PG8_SA(0, 0), a2, 0, last);
;             PG8_WAIT_V(8); PG8_WAIT_L(0); PG8_BAR; PG8_MMA(1, 0, At, B0); PG8_MMA(1, 1, At, B1); PG8_BAR; PG8_SCHED;
;             PG8_LDB(B0, 1, 0); PG8_LDB(B1, 1, 1); PG8_SCHED; PG8_LDA(At, 1, 0); PG8_STAGEA(PG8_SA(0, 1), a2, 1, last);
;             PG8_WAIT_V(8); PG8_WAIT_L(0); PG8_BAR; PG8_MMA(0, 0, At, B0); PG8_MMA(0, 1, At, B1); PG8_BAR; PG8_SCHED;
;             PG8_LDA(At, 1, 1); PG8_STAGE(PG8_SB(1, 0), b3, voffB); PG8_STAGE(PG8_SB(1, 1), b3 + hstep, voffB); PG8_STAGEA(PG8_SA(1, 0), a3, 0, last);
;             PG8_WAIT_V(8); PG8_WAIT_L(0); PG8_BAR; PG8_MMA(1, 0, At, B0); PG8_MMA(1, 1, At, B1); PG8_BAR; PG8_SCHED;
	s_add_i32 s59, s59, s66
	v_lshl_add_u64 v[200:201], v[200:201], 0, s[26:27]
	s_mov_b32 m0, s59
	ds_read_b128 v[184:187], v174 offset:49152
	ds_read_b128 v[188:191], v174 offset:50176
	ds_read_b128 v[192:195], v174 offset:51200
	ds_read_b128 v[196:199], v174 offset:52224
	ds_read_b128 v[204:207], v174 offset:53248
	ds_read_b128 v[208:211], v174 offset:54272
	ds_read_b128 v[212:215], v174 offset:55296
	ds_read_b128 v[216:219], v174 offset:56320
	global_load_lds_dwordx4 v[200:201], off
	s_add_i32 m0, s59, 0x2000
	s_add_u32 s54, s54, 0x80080
	v_lshl_add_u64 v[200:201], v[220:221], 0, s[26:27]
	s_addc_u32 s55, s55, 0
	s_add_i32 s59, s62, s66
	global_load_lds_dwordx4 v[200:201], off
	v_lshl_add_u64 v[200:201], s[54:55], 0, v[148:149]
	s_mov_b32 m0, s59
	s_nop 0
	global_load_lds_dwordx4 v[200:201], off
	v_lshl_add_u64 v[200:201], s[54:55], 0, v[152:153]
	s_add_i32 m0, s59, 0x2000
	s_nop 0
	global_load_lds_dwordx4 v[200:201], off
	v_lshl_add_u64 v[200:201], v[222:223], 0, s[26:27]
	s_mov_b32 m0, s74
	s_nop 0
	global_load_lds_dwordx4 v[200:201], off
	v_lshl_add_u64 v[200:201], v[224:225], 0, s[26:27]
	s_mov_b32 m0, s75
	s_nop 0
	global_load_lds_dwordx4 v[200:201], off
	s_waitcnt vmcnt(8) lgkmcnt(0)
	s_barrier
	s_setprio 1
	v_mfma_f32_16x16x32_bf16 v[58:61], v[130:133], v[184:187], v[58:61]
	v_mfma_f32_16x16x32_bf16 v[62:65], v[138:141], v[184:187], v[62:65]
	v_mfma_f32_16x16x32_bf16 v[42:45], v[130:133], v[192:195], v[42:45]
	v_mfma_f32_16x16x32_bf16 v[46:49], v[138:141], v[192:195], v[46:49]
	v_mfma_f32_16x16x32_bf16 v[18:21], v[130:133], v[204:207], v[18:21]
	v_mfma_f32_16x16x32_bf16 v[22:25], v[138:141], v[204:207], v[22:25]
	v_mfma_f32_16x16x32_bf16 v[6:9], v[130:133], v[212:215], v[6:9]
	v_mfma_f32_16x16x32_bf16 v[14:17], v[138:141], v[212:215], v[14:17]
	v_mfma_f32_16x16x32_bf16 v[58:61], v[134:137], v[188:191], v[58:61]
	v_mfma_f32_16x16x32_bf16 v[62:65], v[142:145], v[188:191], v[62:65]
	v_mfma_f32_16x16x32_bf16 v[42:45], v[134:137], v[196:199], v[42:45]
	v_mfma_f32_16x16x32_bf16 v[46:49], v[142:145], v[196:199], v[46:49]
	v_mfma_f32_16x16x32_bf16 v[18:21], v[134:137], v[208:211], v[18:21]
	v_mfma_f32_16x16x32_bf16 v[22:25], v[142:145], v[208:211], v[22:25]
	v_mfma_f32_16x16x32_bf16 v[6:9], v[134:137], v[216:219], v[6:9]
	v_mfma_f32_16x16x32_bf16 v[14:17], v[142:145], v[216:219], v[14:17]
	v_mfma_f32_16x16x32_bf16 v[50:53], v[162:165], v[184:187], v[50:53]
	v_mfma_f32_16x16x32_bf16 v[54:57], v[176:179], v[184:187], v[54:57]
	v_mfma_f32_16x16x32_bf16 v[34:37], v[162:165], v[192:195], v[34:37]
	v_mfma_f32_16x16x32_bf16 v[38:41], v[176:179], v[192:195], v[38:41]
	v_mfma_f32_16x16x32_bf16 v[26:29], v[162:165], v[204:207], v[26:29]
	v_mfma_f32_16x16x32_bf16 v[30:33], v[176:179], v[204:207], v[30:33]
	v_mfma_f32_16x16x32_bf16 v[10:13], v[162:165], v[212:215], v[10:13]
	v_mfma_f32_16x16x32_bf16 v[2:5], v[176:179], v[212:215], v[2:5]
	v_mfma_f32_16x16x32_bf16 v[50:53], v[166:169], v[188:191], v[50:53]
	v_mfma_f32_16x16x32_bf16 v[54:57], v[180:183], v[188:191], v[54:57]
	v_mfma_f32_16x16x32_bf16 v[34:37], v[166:169], v[196:199], v[34:37]
	v_mfma_f32_16x16x32_bf16 v[38:41], v[180:183], v[196:199], v[38:41]
	v_mfma_f32_16x16x32_bf16 v[26:29], v[166:169], v[208:211], v[26:29]
	v_mfma_f32_16x16x32_bf16 v[30:33], v[180:183], v[208:211], v[30:33]
	v_mfma_f32_16x16x32_bf16 v[10:13], v[166:169], v[216:219], v[10:13]
	v_mfma_f32_16x16x32_bf16 v[2:5], v[180:183], v[216:219], v[2:5]
	s_setprio 0
	s_barrier
	s_add_i32 s49, s49, 2
	s_add_u32 s10, s10, 0x100
	s_addc_u32 s11, s11, 0
	s_add_u32 s37, s37, 0x100
	s_addc_u32 s47, s47, 0
	s_cmp_gt_u32 s49, 29
	s_cbranch_scc0 .LBB0_110
	s_and_b64 vcc, exec, s[38:39]
	s_cbranch_vccz .LBB0_113
	s_barrier

; #define PG8_STAGE(bufoff, gbase, voff) do { _Pragma("unroll") for (int _i = 0; _i < 2; ++_i) \
;         __builtin_amdgcn_global_load_lds((const unsigned*)((const char*)(gbase) + (voff)[_i]), (PG8_LAS unsigned*)(lds + (bufoff) + ldsw + _i * 8192), 16, 0, 0); } while (0)
; #define PG8_LDA(dst, b, h) do { _Pragma("unroll") for (int m = 0; m < 4; ++m) _Pragma("unroll") for (int k = 0; k < 2; ++k) dst[m][k] = *(const PG8_LAS bf16x8*)(lds + PG8_SA(b, h) + aoff + m * 2048 + k * 1024); } while (0)
; #define PG8_LDB(dst, b, h) do { _Pragma("unroll") for (int n = 0; n < 2; ++n) _Pragma("unroll") for (int k = 0; k < 2; ++k) dst[n][k] = *(const PG8_LAS bf16x8*)(lds + PG8_SB(b, h) + boff + n * 2048 + k * 1024); } while (0)
; #define PG8_MMA(ai, bj, At, Bt) do { __builtin_amdgcn_s_setprio(1); _Pragma("unroll") for (int m = 0; m < 4; ++m) _Pragma("unroll") for (int n = 0; n < 2; ++n) _Pragma("unroll") for (int k = 0; k < 2; ++k) \
;         acc[ai][bj][m][n] = __builtin_amdgcn_mfma_f32_16x16x32_bf16(Bt[n][k], At[m][k], acc[ai][bj][m][n], 0, 0, 0); __builtin_amdgcn_s_setprio(0); } while (0)
; #define PG8_WAIT_V(n) asm volatile("s_waitcnt vmcnt(" #n ")" ::: "memory")
; #define PG8_WAIT_L(n) asm volatile("s_waitcnt lgkmcnt(" #n ")" ::: "memory")
; template <class Epi, class Sched, bool ALIGN_EPI = false, bool SP2 = false>
; __device__ __forceinline__ void gemm_phase(PG8_LAS unsigned char* lds, const Gemm g, const Sched& S, const Epi& E) {
;     ...
;         for (; t < tend; t += 2) {
;             const bool last = (t == nt - 2);
;             const char* a1 = cA + (size_t)(t + 1) * kstep;
;             const char* a2 = last ? nA : cA + (size_t)(t + 2) * kstep; const char* b2 = last ? nB : cB + (size_t)(t + 2) * kstep;
;             const char* a3 = a2 + kstep; const char* b3 = b2 + kstep;
;             if (last && has_next) S.a_ready(nxt);
;             if constexpr (SP2) {
;             PG8_LDB(B0, 0, 0); PG8_LDB(B1, 0, 1); PG8_SCHED; PG8_LDA(At, 0, 0); PG8_STAGEA(PG8_SA(1, 1), a1, 1, false);
;             PG8_WAIT_V(8); PG8_WAIT_L(0); PG8_BAR; PG8_MMA(0, 0, At, B0); PG8_MMA(0, 1, At, B1); PG8_BAR; PG8_SCHED;
;             PG8_LDA(At, 0, 1); PG8_STAGE(PG8_SB(0, 0), b2, voffB); PG8_STAGE(PG8_SB(0, 1), b2 + hstep, voffB); PG8_STAGEA(PG8_SA(0, 0), a2, 0, last);
;             PG8_WAIT_V(8); PG8_WAIT_L(0); PG8_BAR; PG8_MMA(1, 0, At, B0); PG8_MMA(1, 1, At, B1); PG8_BAR; PG8_SCHED;
.LBB0_383:
	s_nop 0
	v_add_u32_e32 v142, s79, v173
	v_add_u32_e32 v170, s80, v173
	ds_read_b128 v[130:133], v142
	ds_read_b128 v[134:137], v142 offset:1024
	ds_read_b128 v[138:141], v142 offset:2048
	ds_read_b128 v[142:145], v142 offset:3072
	ds_read_b128 v[146:149], v170
	ds_read_b128 v[150:153], v170 offset:1024
	ds_read_b128 v[154:157], v170 offset:2048
	ds_read_b128 v[176:179], v170 offset:3072
	s_add_i32 s58, s56, 1
	s_ashr_i32 s59, s58, 31
	s_mov_b32 s62, s56
	s_add_i32 s56, s56, 2
	s_lshl_b64 s[96:97], s[58:59], 7
	s_cmp_eq_u32 s62, 30
	s_cselect_b32 s63, s9, s36
	s_cselect_b32 s62, s49, s19
	s_cselect_b32 s59, s89, s57
	s_cselect_b32 s58, s90, s37
	s_add_u32 s95, s10, s96
	s_addc_u32 s97, s11, s97
	s_add_u32 s96, s95, 0x80000
	s_addc_u32 s97, s97, 0
	v_lshl_add_u64 v[170:171], s[96:97], 0, v[158:159]
	s_add_i32 m0, s66, 0xc000
	ds_read_b128 v[180:183], v174
	ds_read_b128 v[184:187], v174 offset:1024
	ds_read_b128 v[188:191], v174 offset:2048
	ds_read_b128 v[192:195], v174 offset:3072
	ds_read_b128 v[196:199], v174 offset:4096
	ds_read_b128 v[204:207], v174 offset:5120
	ds_read_b128 v[208:211], v174 offset:6144
	ds_read_b128 v[212:215], v174 offset:7168
	global_load_lds_dwordx4 v[170:171], off
	v_lshl_add_u64 v[170:171], s[96:97], 0, v[162:163]
	s_add_i32 m0, s66, 0xe000
	s_nop 0
	global_load_lds_dwordx4 v[170:171], off
	s_waitcnt vmcnt(8) lgkmcnt(0)
	s_barrier
	s_setprio 1
	v_mfma_f32_16x16x32_bf16 v[118:121], v[130:133], v[180:183], v[118:121]
	v_mfma_f32_16x16x32_bf16 v[114:117], v[138:141], v[180:183], v[114:117]
	v_mfma_f32_16x16x32_bf16 v[102:105], v[130:133], v[188:191], v[102:105]
	v_mfma_f32_16x16x32_bf16 v[98:101], v[138:141], v[188:191], v[98:101]
	v_mfma_f32_16x16x32_bf16 v[86:89], v[130:133], v[196:199], v[86:89]
	v_mfma_f32_16x16x32_bf16 v[82:85], v[138:141], v[196:199], v[82:85]
	v_mfma_f32_16x16x32_bf16 v[70:73], v[130:133], v[208:211], v[70:73]
	v_mfma_f32_16x16x32_bf16 v[66:69], v[138:141], v[208:211], v[66:69]
	v_mfma_f32_16x16x32_bf16 v[118:121], v[134:137], v[184:187], v[118:121]
	v_mfma_f32_16x16x32_bf16 v[114:117], v[142:145], v[184:187], v[114:117]
	v_mfma_f32_16x16x32_bf16 v[102:105], v[134:137], v[192:195], v[102:105]
	v_mfma_f32_16x16x32_bf16 v[98:101], v[142:145], v[192:195], v[98:101]
	v_mfma_f32_16x16x32_bf16 v[86:89], v[134:137], v[204:207], v[86:89]
	v_mfma_f32_16x16x32_bf16 v[82:85], v[142:145], v[204:207], v[82:85]
	v_mfma_f32_16x16x32_bf16 v[70:73], v[134:137], v[212:215], v[70:73]
	v_mfma_f32_16x16x32_bf16 v[66:69], v[142:145], v[212:215], v[66:69]
	v_mfma_f32_16x16x32_bf16 v[126:129], v[146:149], v[180:183], v[126:129]
	v_mfma_f32_16x16x32_bf16 v[122:125], v[154:157], v[180:183], v[122:125]
	v_mfma_f32_16x16x32_bf16 v[110:113], v[146:149], v[188:191], v[110:113]
	v_mfma_f32_16x16x32_bf16 v[106:109], v[154:157], v[188:191], v[106:109]
	v_mfma_f32_16x16x32_bf16 v[94:97], v[146:149], v[196:199], v[94:97]
	v_mfma_f32_16x16x32_bf16 v[90:93], v[154:157], v[196:199], v[90:93]
	v_mfma_f32_16x16x32_bf16 v[78:81], v[146:149], v[208:211], v[78:81]
	v_mfma_f32_16x16x32_bf16 v[74:77], v[154:157], v[208:211], v[74:77]
	v_mfma_f32_16x16x32_bf16 v[126:129], v[150:153], v[184:187], v[126:129]
	v_mfma_f32_16x16x32_bf16 v[122:125], v[176:179], v[184:187], v[122:125]
	v_mfma_f32_16x16x32_bf16 v[110:113], v[150:153], v[192:195], v[110:113]
	v_mfma_f32_16x16x32_bf16 v[106:109], v[176:179], v[192:195], v[106:109]
	v_mfma_f32_16x16x32_bf16 v[94:97], v[150:153], v[204:207], v[94:97]
	v_mfma_f32_16x16x32_bf16 v[90:93], v[176:179], v[204:207], v[90:93]
	v_mfma_f32_16x16x32_bf16 v[78:81], v[150:153], v[212:215], v[78:81]
	v_mfma_f32_16x16x32_bf16 v[74:77], v[176:179], v[212:215], v[74:77]
	s_setprio 0
	s_barrier
	s_nop 0
	s_add_i32 s95, s79, s65
	v_lshl_add_u64 v[170:171], s[58:59], 0, v[160:161]
	s_mov_b32 m0, s95
	ds_read_b128 v[180:183], v174 offset:16384
	ds_read_b128 v[184:187], v174 offset:17408
	ds_read_b128 v[188:191], v174 offset:18432
	ds_read_b128 v[192:195], v174 offset:19456
	ds_read_b128 v[196:199], v174 offset:20480
	ds_read_b128 v[204:207], v174 offset:21504
	ds_read_b128 v[208:211], v174 offset:22528
	ds_read_b128 v[212:215], v174 offset:23552
	global_load_lds_dwordx4 v[170:171], off
	s_add_i32 m0, s95, 0x2000
	s_add_u32 s96, s58, 0x80000
	v_lshl_add_u64 v[200:201], s[58:59], 0, v[164:165]
	s_addc_u32 s97, s59, 0
	s_add_i32 s95, s80, s65
	global_load_lds_dwordx4 v[200:201], off
	v_lshl_add_u64 v[216:217], s[96:97], 0, v[160:161]
	s_mov_b32 m0, s95
	v_lshl_add_u64 v[218:219], s[62:63], 0, v[162:163]
	global_load_lds_dwordx4 v[216:217], off
	v_lshl_add_u64 v[216:217], s[96:97], 0, v[164:165]
	s_add_i32 m0, s95, 0x2000
	s_nop 0
	global_load_lds_dwordx4 v[216:217], off
	v_lshl_add_u64 v[216:217], s[62:63], 0, v[158:159]
	s_mov_b32 m0, s66
	s_nop 0
	global_load_lds_dwordx4 v[216:217], off
	s_mov_b32 m0, s67
	s_nop 0
	global_load_lds_dwordx4 v[218:219], off
	s_waitcnt vmcnt(8) lgkmcnt(0)
	s_barrier
; #define PG8_LDA(dst, b, h) do { _Pragma("unroll") for (int m = 0; m < 4; ++m) _Pragma("unroll") for (int k = 0; k < 2; ++k) dst[m][k] = *(const PG8_LAS bf16x8*)(lds + PG8_SA(b, h) + aoff + m * 2048 + k * 1024); } while (0)
; #define PG8_LDB(dst, b, h) do { _Pragma("unroll") for (int n = 0; n < 2; ++n) _Pragma("unroll") for (int k = 0; k < 2; ++k) dst[n][k] = *(const PG8_LAS bf16x8*)(lds + PG8_SB(b, h) + boff + n * 2048 + k * 1024); } while (0)
; #define PG8_MMA(ai, bj, At, Bt) do { __builtin_amdgcn_s_setprio(1); _Pragma("unroll") for (int m = 0; m < 4; ++m) _Pragma("unroll") for (int n = 0; n < 2; ++n) _Pragma("unroll") for (int k = 0; k < 2; ++k) \
;         acc[ai][bj][m][n] = __builtin_amdgcn_mfma_f32_16x16x32_bf16(Bt[n][k], At[m][k], acc[ai][bj][m][n], 0, 0, 0); __builtin_amdgcn_s_setprio(0); } while (0)
; #define PG8_WAIT_V(n) asm volatile("s_waitcnt vmcnt(" #n ")" ::: "memory")
; #define PG8_WAIT_L(n) asm volatile("s_waitcnt lgkmcnt(" #n ")" ::: "memory")
; #define PG8_BAR __builtin_amdgcn_s_barrier()
; #define PG8_SCHED __builtin_amdgcn_sched_barrier(0)
; template <class Epi, class Sched, bool ALIGN_EPI = false, bool SP2 = false>
; __device__ __forceinline__ void gemm_phase(PG8_LAS unsigned char* lds, const Gemm g, const Sched& S, const Epi& E) {
;     ...
;             PG8_WAIT_V(8); PG8_WAIT_L(0); PG8_BAR; PG8_MMA(1, 0, At, B0); PG8_MMA(1, 1, At, B1); PG8_BAR; PG8_SCHED;
;             PG8_LDB(B0, 1, 0); PG8_LDB(B1, 1, 1); PG8_SCHED; PG8_LDA(At, 1, 0); PG8_STAGEA(PG8_SA(0, 1), a2, 1, last);
;             PG8_WAIT_V(8); PG8_WAIT_L(0); PG8_BAR; PG8_MMA(0, 0, At, B0); PG8_MMA(0, 1, At, B1); PG8_BAR; PG8_SCHED;
	s_setprio 1
	v_mfma_f32_16x16x32_bf16 v[54:57], v[130:133], v[180:183], v[54:57]
	v_mfma_f32_16x16x32_bf16 v[50:53], v[138:141], v[180:183], v[50:53]
	v_mfma_f32_16x16x32_bf16 v[38:41], v[130:133], v[188:191], v[38:41]
	v_mfma_f32_16x16x32_bf16 v[34:37], v[138:141], v[188:191], v[34:37]
	v_mfma_f32_16x16x32_bf16 v[22:25], v[130:133], v[196:199], v[22:25]
	v_mfma_f32_16x16x32_bf16 v[18:21], v[138:141], v[196:199], v[18:21]
	v_mfma_f32_16x16x32_bf16 v[10:13], v[130:133], v[208:211], v[10:13]
	v_mfma_f32_16x16x32_bf16 v[6:9], v[138:141], v[208:211], v[6:9]
	v_mfma_f32_16x16x32_bf16 v[54:57], v[134:137], v[184:187], v[54:57]
	v_mfma_f32_16x16x32_bf16 v[50:53], v[142:145], v[184:187], v[50:53]
	v_mfma_f32_16x16x32_bf16 v[38:41], v[134:137], v[192:195], v[38:41]
	v_mfma_f32_16x16x32_bf16 v[34:37], v[142:145], v[192:195], v[34:37]
	v_mfma_f32_16x16x32_bf16 v[22:25], v[134:137], v[204:207], v[22:25]
	v_mfma_f32_16x16x32_bf16 v[18:21], v[142:145], v[204:207], v[18:21]
	v_mfma_f32_16x16x32_bf16 v[10:13], v[134:137], v[212:215], v[10:13]
	v_mfma_f32_16x16x32_bf16 v[6:9], v[142:145], v[212:215], v[6:9]
	v_mfma_f32_16x16x32_bf16 v[62:65], v[146:149], v[180:183], v[62:65]
	v_mfma_f32_16x16x32_bf16 v[58:61], v[154:157], v[180:183], v[58:61]
	v_mfma_f32_16x16x32_bf16 v[46:49], v[146:149], v[188:191], v[46:49]
	v_mfma_f32_16x16x32_bf16 v[42:45], v[154:157], v[188:191], v[42:45]
	v_mfma_f32_16x16x32_bf16 v[30:33], v[146:149], v[196:199], v[30:33]
	v_mfma_f32_16x16x32_bf16 v[26:29], v[154:157], v[196:199], v[26:29]
	v_mfma_f32_16x16x32_bf16 v[14:17], v[146:149], v[208:211], v[14:17]
	v_mfma_f32_16x16x32_bf16 v[2:5], v[154:157], v[208:211], v[2:5]
	v_mfma_f32_16x16x32_bf16 v[62:65], v[150:153], v[184:187], v[62:65]
	v_mfma_f32_16x16x32_bf16 v[58:61], v[176:179], v[184:187], v[58:61]
	v_mfma_f32_16x16x32_bf16 v[46:49], v[150:153], v[192:195], v[46:49]
	v_mfma_f32_16x16x32_bf16 v[42:45], v[176:179], v[192:195], v[42:45]
	v_mfma_f32_16x16x32_bf16 v[30:33], v[150:153], v[204:207], v[30:33]
	v_mfma_f32_16x16x32_bf16 v[26:29], v[176:179], v[204:207], v[26:29]
	v_mfma_f32_16x16x32_bf16 v[14:17], v[150:153], v[212:215], v[14:17]
	v_mfma_f32_16x16x32_bf16 v[2:5], v[176:179], v[212:215], v[2:5]
	s_setprio 0
	s_barrier
	s_nop 0
	s_add_i32 s95, 0, 0x18000
	s_add_i32 s96, 0, 0x1c000
	v_add_u32_e32 v142, s95, v173
	v_add_u32_e32 v175, s96, v173
	ds_read_b128 v[130:133], v142
	ds_read_b128 v[134:137], v142 offset:1024
	ds_read_b128 v[138:141], v142 offset:2048
	ds_read_b128 v[142:145], v142 offset:3072
	ds_read_b128 v[146:149], v175
	ds_read_b128 v[150:153], v175 offset:1024
	ds_read_b128 v[154:157], v175 offset:2048
	ds_read_b128 v[176:179], v175 offset:3072
	s_add_u32 s62, s62, 0x80000
	s_addc_u32 s63, s63, 0
	s_mov_b32 m0, s68
	v_lshl_add_u64 v[220:221], s[62:63], 0, v[158:159]
	ds_read_b128 v[180:183], v174 offset:32768
	ds_read_b128 v[184:187], v174 offset:33792
	ds_read_b128 v[188:191], v174 offset:34816
	ds_read_b128 v[192:195], v174 offset:35840
	ds_read_b128 v[196:199], v174 offset:36864
	ds_read_b128 v[204:207], v174 offset:37888
	ds_read_b128 v[208:211], v174 offset:38912
	ds_read_b128 v[212:215], v174 offset:39936
	global_load_lds_dwordx4 v[220:221], off
	v_lshl_add_u64 v[220:221], s[62:63], 0, v[162:163]
	s_mov_b32 m0, s69
	s_nop 0
	global_load_lds_dwordx4 v[220:221], off
	s_waitcnt vmcnt(8) lgkmcnt(0)
	s_barrier
	s_setprio 1
	v_mfma_f32_16x16x32_bf16 v[118:121], v[130:133], v[180:183], v[118:121]
	v_mfma_f32_16x16x32_bf16 v[114:117], v[138:141], v[180:183], v[114:117]
	v_mfma_f32_16x16x32_bf16 v[102:105], v[130:133], v[188:191], v[102:105]
	v_mfma_f32_16x16x32_bf16 v[98:101], v[138:141], v[188:191], v[98:101]
	v_mfma_f32_16x16x32_bf16 v[86:89], v[130:133], v[196:199], v[86:89]
	v_mfma_f32_16x16x32_bf16 v[82:85], v[138:141], v[196:199], v[82:85]
	v_mfma_f32_16x16x32_bf16 v[70:73], v[130:133], v[208:211], v[70:73]
	v_mfma_f32_16x16x32_bf16 v[66:69], v[138:141], v[208:211], v[66:69]
	v_mfma_f32_16x16x32_bf16 v[118:121], v[134:137], v[184:187], v[118:121]
	v_mfma_f32_16x16x32_bf16 v[114:117], v[142:145], v[184:187], v[114:117]
	v_mfma_f32_16x16x32_bf16 v[102:105], v[134:137], v[192:195], v[102:105]
	v_mfma_f32_16x16x32_bf16 v[98:101], v[142:145], v[192:195], v[98:101]
	v_mfma_f32_16x16x32_bf16 v[86:89], v[134:137], v[204:207], v[86:89]
	v_mfma_f32_16x16x32_bf16 v[82:85], v[142:145], v[204:207], v[82:85]
	v_mfma_f32_16x16x32_bf16 v[70:73], v[134:137], v[212:215], v[70:73]
	v_mfma_f32_16x16x32_bf16 v[66:69], v[142:145], v[212:215], v[66:69]
	v_mfma_f32_16x16x32_bf16 v[126:129], v[146:149], v[180:183], v[126:129]
	v_mfma_f32_16x16x32_bf16 v[122:125], v[154:157], v[180:183], v[122:125]
	v_mfma_f32_16x16x32_bf16 v[110:113], v[146:149], v[188:191], v[110:113]
	v_mfma_f32_16x16x32_bf16 v[106:109], v[154:157], v[188:191], v[106:109]
	v_mfma_f32_16x16x32_bf16 v[94:97], v[146:149], v[196:199], v[94:97]
	v_mfma_f32_16x16x32_bf16 v[90:93], v[154:157], v[196:199], v[90:93]
	v_mfma_f32_16x16x32_bf16 v[78:81], v[146:149], v[208:211], v[78:81]
	v_mfma_f32_16x16x32_bf16 v[74:77], v[154:157], v[208:211], v[74:77]
	v_mfma_f32_16x16x32_bf16 v[126:129], v[150:153], v[184:187], v[126:129]
	v_mfma_f32_16x16x32_bf16 v[122:125], v[176:179], v[184:187], v[122:125]
	v_mfma_f32_16x16x32_bf16 v[110:113], v[150:153], v[192:195], v[110:113]
	v_mfma_f32_16x16x32_bf16 v[106:109], v[176:179], v[192:195], v[106:109]
	v_mfma_f32_16x16x32_bf16 v[94:97], v[150:153], v[204:207], v[94:97]
	v_mfma_f32_16x16x32_bf16 v[90:93], v[176:179], v[204:207], v[90:93]
	v_mfma_f32_16x16x32_bf16 v[78:81], v[150:153], v[212:215], v[78:81]
	v_mfma_f32_16x16x32_bf16 v[74:77], v[176:179], v[212:215], v[74:77]
	s_setprio 0
	s_barrier
; #define PG8_STAGE(bufoff, gbase, voff) do { _Pragma("unroll") for (int _i = 0; _i < 2; ++_i) \
;         __builtin_amdgcn_global_load_lds((const unsigned*)((const char*)(gbase) + (voff)[_i]), (PG8_LAS unsigned*)(lds + (bufoff) + ldsw + _i * 8192), 16, 0, 0); } while (0)
; #define PG8_LDA(dst, b, h) do { _Pragma("unroll") for (int m = 0; m < 4; ++m) _Pragma("unroll") for (int k = 0; k < 2; ++k) dst[m][k] = *(const PG8_LAS bf16x8*)(lds + PG8_SA(b, h) + aoff + m * 2048 + k * 1024); } while (0)
; #define PG8_MMA(ai, bj, At, Bt) do { __builtin_amdgcn_s_setprio(1); _Pragma("unroll") for (int m = 0; m < 4; ++m) _Pragma("unroll") for (int n = 0; n < 2; ++n) _Pragma("unroll") for (int k = 0; k < 2; ++k) \
;         acc[ai][bj][m][n] = __builtin_amdgcn_mfma_f32_16x16x32_bf16(Bt[n][k], At[m][k], acc[ai][bj][m][n], 0, 0, 0); __builtin_amdgcn_s_setprio(0); } while (0)
; #define PG8_WAIT_V(n) asm volatile("s_waitcnt vmcnt(" #n ")" ::: "memory")
; #define PG8_WAIT_L(n) asm volatile("s_waitcnt lgkmcnt(" #n ")" ::: "memory")
; #define PG8_BAR __builtin_amdgcn_s_barrier()
; #define PG8_SCHED __builtin_amdgcn_sched_barrier(0)
; template <class Epi, class Sched, bool ALIGN_EPI = false, bool SP2 = false>
; __device__ __forceinline__ void gemm_phase(PG8_LAS unsigned char* lds, const Gemm g, const Sched& S, const Epi& E) {
;     ...
;         for (; t < tend; t += 2) {
;             const bool last = (t == nt - 2);
;             const char* a1 = cA + (size_t)(t + 1) * kstep;
;             const char* a2 = last ? nA : cA + (size_t)(t + 2) * kstep; const char* b2 = last ? nB : cB + (size_t)(t + 2) * kstep;
;     ...
;             PG8_LDA(At, 1, 1); PG8_STAGE(PG8_SB(1, 0), b3, voffB); PG8_STAGE(PG8_SB(1, 1), b3 + hstep, voffB); PG8_STAGEA(PG8_SA(1, 0), a3, 0, last);
;             PG8_WAIT_V(8); PG8_WAIT_L(0); PG8_BAR; PG8_MMA(1, 0, At, B0); PG8_MMA(1, 1, At, B1); PG8_BAR; PG8_SCHED;
	s_add_i32 s62, s95, s65
	v_lshl_add_u64 v[170:171], v[170:171], 0, s[26:27]
	s_mov_b32 m0, s62
	ds_read_b128 v[180:183], v174 offset:49152
	ds_read_b128 v[184:187], v174 offset:50176
	ds_read_b128 v[188:191], v174 offset:51200
	ds_read_b128 v[192:195], v174 offset:52224
	ds_read_b128 v[196:199], v174 offset:53248
	ds_read_b128 v[204:207], v174 offset:54272
	ds_read_b128 v[208:211], v174 offset:55296
	ds_read_b128 v[212:215], v174 offset:56320
	global_load_lds_dwordx4 v[170:171], off
	s_add_i32 m0, s62, 0x2000
	s_add_u32 s58, s58, 0x80080
	v_lshl_add_u64 v[170:171], v[200:201], 0, s[26:27]
	s_addc_u32 s59, s59, 0
	s_add_i32 s62, s96, s65
	global_load_lds_dwordx4 v[170:171], off
	v_lshl_add_u64 v[170:171], s[58:59], 0, v[160:161]
	s_mov_b32 m0, s62
	s_nop 0
	global_load_lds_dwordx4 v[170:171], off
	v_lshl_add_u64 v[170:171], s[58:59], 0, v[164:165]
	s_add_i32 m0, s62, 0x2000
	s_nop 0
	global_load_lds_dwordx4 v[170:171], off
	v_lshl_add_u64 v[170:171], v[216:217], 0, s[26:27]
	s_mov_b32 m0, s76
	s_nop 0
	global_load_lds_dwordx4 v[170:171], off
	v_lshl_add_u64 v[170:171], v[218:219], 0, s[26:27]
	s_mov_b32 m0, s77
	s_nop 0
	global_load_lds_dwordx4 v[170:171], off
	s_waitcnt vmcnt(8) lgkmcnt(0)
	s_barrier
	s_setprio 1
	v_mfma_f32_16x16x32_bf16 v[54:57], v[130:133], v[180:183], v[54:57]
	v_mfma_f32_16x16x32_bf16 v[50:53], v[138:141], v[180:183], v[50:53]
	v_mfma_f32_16x16x32_bf16 v[38:41], v[130:133], v[188:191], v[38:41]
	v_mfma_f32_16x16x32_bf16 v[34:37], v[138:141], v[188:191], v[34:37]
	v_mfma_f32_16x16x32_bf16 v[22:25], v[130:133], v[196:199], v[22:25]
	v_mfma_f32_16x16x32_bf16 v[18:21], v[138:141], v[196:199], v[18:21]
	v_mfma_f32_16x16x32_bf16 v[10:13], v[130:133], v[208:211], v[10:13]
	v_mfma_f32_16x16x32_bf16 v[6:9], v[138:141], v[208:211], v[6:9]
	v_mfma_f32_16x16x32_bf16 v[54:57], v[134:137], v[184:187], v[54:57]
	v_mfma_f32_16x16x32_bf16 v[50:53], v[142:145], v[184:187], v[50:53]
	v_mfma_f32_16x16x32_bf16 v[38:41], v[134:137], v[192:195], v[38:41]
	v_mfma_f32_16x16x32_bf16 v[34:37], v[142:145], v[192:195], v[34:37]
	v_mfma_f32_16x16x32_bf16 v[22:25], v[134:137], v[204:207], v[22:25]
	v_mfma_f32_16x16x32_bf16 v[18:21], v[142:145], v[204:207], v[18:21]
	v_mfma_f32_16x16x32_bf16 v[10:13], v[134:137], v[212:215], v[10:13]
	v_mfma_f32_16x16x32_bf16 v[6:9], v[142:145], v[212:215], v[6:9]
	v_mfma_f32_16x16x32_bf16 v[62:65], v[146:149], v[180:183], v[62:65]
	v_mfma_f32_16x16x32_bf16 v[58:61], v[154:157], v[180:183], v[58:61]
	v_mfma_f32_16x16x32_bf16 v[46:49], v[146:149], v[188:191], v[46:49]
	v_mfma_f32_16x16x32_bf16 v[42:45], v[154:157], v[188:191], v[42:45]
	v_mfma_f32_16x16x32_bf16 v[30:33], v[146:149], v[196:199], v[30:33]
	v_mfma_f32_16x16x32_bf16 v[26:29], v[154:157], v[196:199], v[26:29]
	v_mfma_f32_16x16x32_bf16 v[14:17], v[146:149], v[208:211], v[14:17]
	v_mfma_f32_16x16x32_bf16 v[2:5], v[154:157], v[208:211], v[2:5]
	v_mfma_f32_16x16x32_bf16 v[62:65], v[150:153], v[184:187], v[62:65]
	v_mfma_f32_16x16x32_bf16 v[58:61], v[176:179], v[184:187], v[58:61]
	v_mfma_f32_16x16x32_bf16 v[46:49], v[150:153], v[192:195], v[46:49]
	v_mfma_f32_16x16x32_bf16 v[42:45], v[176:179], v[192:195], v[42:45]
	v_mfma_f32_16x16x32_bf16 v[30:33], v[150:153], v[204:207], v[30:33]
	v_mfma_f32_16x16x32_bf16 v[26:29], v[176:179], v[204:207], v[26:29]
	v_mfma_f32_16x16x32_bf16 v[14:17], v[150:153], v[212:215], v[14:17]
	v_mfma_f32_16x16x32_bf16 v[2:5], v[176:179], v[212:215], v[2:5]
	s_setprio 0
	s_barrier
	s_add_u32 s19, s19, 0x100
	s_addc_u32 s36, s36, 0
	s_add_u32 s37, s37, 0x100
	s_addc_u32 s57, s57, 0
	s_cmp_lt_i32 s56, s18
	s_cbranch_scc1 .LBB0_383
	s_nop 0

; #define PG8_STAGE(bufoff, gbase, voff) do { _Pragma("unroll") for (int _i = 0; _i < 2; ++_i) \
;         __builtin_amdgcn_global_load_lds((const unsigned*)((const char*)(gbase) + (voff)[_i]), (PG8_LAS unsigned*)(lds + (bufoff) + ldsw + _i * 8192), 16, 0, 0); } while (0)
; #define PG8_LDA(dst, b, h) do { _Pragma("unroll") for (int m = 0; m < 4; ++m) _Pragma("unroll") for (int k = 0; k < 2; ++k) dst[m][k] = *(const PG8_LAS bf16x8*)(lds + PG8_SA(b, h) + aoff + m * 2048 + k * 1024); } while (0)
; #define PG8_LDB(dst, b, h) do { _Pragma("unroll") for (int n = 0; n < 2; ++n) _Pragma("unroll") for (int k = 0; k < 2; ++k) dst[n][k] = *(const PG8_LAS bf16x8*)(lds + PG8_SB(b, h) + boff + n * 2048 + k * 1024); } while (0)
; #define PG8_MMA(ai, bj, At, Bt) do { __builtin_amdgcn_s_setprio(1); _Pragma("unroll") for (int m = 0; m < 4; ++m) _Pragma("unroll") for (int n = 0; n < 2; ++n) _Pragma("unroll") for (int k = 0; k < 2; ++k) \
;         acc[ai][bj][m][n] = __builtin_amdgcn_mfma_f32_16x16x32_bf16(Bt[n][k], At[m][k], acc[ai][bj][m][n], 0, 0, 0); __builtin_amdgcn_s_setprio(0); } while (0)
; #define PG8_WAIT_V(n) asm volatile("s_waitcnt vmcnt(" #n ")" ::: "memory")
; #define PG8_WAIT_L(n) asm volatile("s_waitcnt lgkmcnt(" #n ")" ::: "memory")
; template <class Epi, class Sched, bool ALIGN_EPI = false, bool SP2 = false>
; __device__ __forceinline__ void gemm_phase(PG8_LAS unsigned char* lds, const Gemm g, const Sched& S, const Epi& E) {
;     ...
;         for (; t < tend; t += 2) {
;             const bool last = (t == nt - 2);
;             const char* a1 = cA + (size_t)(t + 1) * kstep;
;             const char* a2 = last ? nA : cA + (size_t)(t + 2) * kstep; const char* b2 = last ? nB : cB + (size_t)(t + 2) * kstep;
;             const char* a3 = a2 + kstep; const char* b3 = b2 + kstep;
;             if (last && has_next) S.a_ready(nxt);
;             if constexpr (SP2) {
;             PG8_LDB(B0, 0, 0); PG8_LDB(B1, 0, 1); PG8_SCHED; PG8_LDA(At, 0, 0); PG8_STAGEA(PG8_SA(1, 1), a1, 1, false);
;             PG8_WAIT_V(8); PG8_WAIT_L(0); PG8_BAR; PG8_MMA(0, 0, At, B0); PG8_MMA(0, 1, At, B1); PG8_BAR; PG8_SCHED;
;             PG8_LDA(At, 0, 1); PG8_STAGE(PG8_SB(0, 0), b2, voffB); PG8_STAGE(PG8_SB(0, 1), b2 + hstep, voffB); PG8_STAGEA(PG8_SA(0, 0), a2, 0, last);
;             PG8_WAIT_V(8); PG8_WAIT_L(0); PG8_BAR; PG8_MMA(1, 0, At, B0); PG8_MMA(1, 1, At, B1); PG8_BAR; PG8_SCHED;
.LBB0_571:
	s_nop 0
	v_add_u32_e32 v162, s66, v150
	v_add_u32_e32 v178, s67, v150
	ds_read_b128 v[146:149], v162
	ds_read_b128 v[154:157], v162 offset:1024
	ds_read_b128 v[158:161], v162 offset:2048
	ds_read_b128 v[162:165], v162 offset:3072
	ds_read_b128 v[166:169], v178
	ds_read_b128 v[170:173], v178 offset:1024
	ds_read_b128 v[174:177], v178 offset:2048
	ds_read_b128 v[178:181], v178 offset:3072
	s_add_u32 s52, s50, 0xfff80080
	s_addc_u32 s53, s51, -1
	s_cmp_eq_u32 s49, 28
	s_cselect_b32 s55, s9, s53
	s_cselect_b32 s54, s11, s52
	s_cselect_b32 s53, s36, s43
	s_cselect_b32 s52, s37, s41
	v_lshl_add_u64 v[216:217], s[50:51], 0, v[138:139]
	s_add_i32 m0, s57, 0xc000
	ds_read_b128 v[182:185], v152
	ds_read_b128 v[186:189], v152 offset:1024
	ds_read_b128 v[190:193], v152 offset:2048
	ds_read_b128 v[194:197], v152 offset:3072
	ds_read_b128 v[198:201], v152 offset:4096
	ds_read_b128 v[204:207], v152 offset:5120
	ds_read_b128 v[208:211], v152 offset:6144
	ds_read_b128 v[212:215], v152 offset:7168
	global_load_lds_dwordx4 v[216:217], off
	v_lshl_add_u64 v[216:217], s[50:51], 0, v[140:141]
	s_add_i32 m0, s57, 0xe000
	s_nop 0
	global_load_lds_dwordx4 v[216:217], off
	s_waitcnt vmcnt(8) lgkmcnt(0)
	s_barrier
	s_setprio 1
	v_mfma_f32_16x16x32_bf16 v[126:129], v[146:149], v[182:185], v[126:129]
	v_mfma_f32_16x16x32_bf16 v[122:125], v[158:161], v[182:185], v[122:125]
	v_mfma_f32_16x16x32_bf16 v[110:113], v[146:149], v[190:193], v[110:113]
	v_mfma_f32_16x16x32_bf16 v[106:109], v[158:161], v[190:193], v[106:109]
	v_mfma_f32_16x16x32_bf16 v[94:97], v[146:149], v[198:201], v[94:97]
	v_mfma_f32_16x16x32_bf16 v[90:93], v[158:161], v[198:201], v[90:93]
	v_mfma_f32_16x16x32_bf16 v[78:81], v[146:149], v[208:211], v[78:81]
	v_mfma_f32_16x16x32_bf16 v[74:77], v[158:161], v[208:211], v[74:77]
	v_mfma_f32_16x16x32_bf16 v[126:129], v[154:157], v[186:189], v[126:129]
	v_mfma_f32_16x16x32_bf16 v[122:125], v[162:165], v[186:189], v[122:125]
	v_mfma_f32_16x16x32_bf16 v[110:113], v[154:157], v[194:197], v[110:113]
	v_mfma_f32_16x16x32_bf16 v[106:109], v[162:165], v[194:197], v[106:109]
	v_mfma_f32_16x16x32_bf16 v[94:97], v[154:157], v[204:207], v[94:97]
	v_mfma_f32_16x16x32_bf16 v[90:93], v[162:165], v[204:207], v[90:93]
	v_mfma_f32_16x16x32_bf16 v[78:81], v[154:157], v[212:215], v[78:81]
	v_mfma_f32_16x16x32_bf16 v[74:77], v[162:165], v[212:215], v[74:77]
	v_mfma_f32_16x16x32_bf16 v[118:121], v[166:169], v[182:185], v[118:121]
	v_mfma_f32_16x16x32_bf16 v[114:117], v[174:177], v[182:185], v[114:117]
	v_mfma_f32_16x16x32_bf16 v[102:105], v[166:169], v[190:193], v[102:105]
	v_mfma_f32_16x16x32_bf16 v[98:101], v[174:177], v[190:193], v[98:101]
	v_mfma_f32_16x16x32_bf16 v[86:89], v[166:169], v[198:201], v[86:89]
	v_mfma_f32_16x16x32_bf16 v[82:85], v[174:177], v[198:201], v[82:85]
	v_mfma_f32_16x16x32_bf16 v[70:73], v[166:169], v[208:211], v[70:73]
	v_mfma_f32_16x16x32_bf16 v[66:69], v[174:177], v[208:211], v[66:69]
	v_mfma_f32_16x16x32_bf16 v[118:121], v[170:173], v[186:189], v[118:121]
	v_mfma_f32_16x16x32_bf16 v[114:117], v[178:181], v[186:189], v[114:117]
	v_mfma_f32_16x16x32_bf16 v[102:105], v[170:173], v[194:197], v[102:105]
	v_mfma_f32_16x16x32_bf16 v[98:101], v[178:181], v[194:197], v[98:101]
	v_mfma_f32_16x16x32_bf16 v[86:89], v[170:173], v[204:207], v[86:89]
	v_mfma_f32_16x16x32_bf16 v[82:85], v[178:181], v[204:207], v[82:85]
	v_mfma_f32_16x16x32_bf16 v[70:73], v[170:173], v[212:215], v[70:73]
	v_mfma_f32_16x16x32_bf16 v[66:69], v[178:181], v[212:215], v[66:69]
	s_setprio 0
	s_barrier
	s_nop 0
	s_add_i32 s69, s66, s56
	v_lshl_add_u64 v[216:217], s[52:53], 0, v[132:133]
	s_mov_b32 m0, s69
	ds_read_b128 v[182:185], v152 offset:16384
	ds_read_b128 v[186:189], v152 offset:17408
	ds_read_b128 v[190:193], v152 offset:18432
	ds_read_b128 v[194:197], v152 offset:19456
	ds_read_b128 v[198:201], v152 offset:20480
	ds_read_b128 v[204:207], v152 offset:21504
	ds_read_b128 v[208:211], v152 offset:22528
	ds_read_b128 v[212:215], v152 offset:23552
	global_load_lds_dwordx4 v[216:217], off
	s_add_i32 m0, s69, 0x2000
	s_add_u32 s74, s52, 0x80000
	v_lshl_add_u64 v[218:219], s[52:53], 0, v[136:137]
	s_addc_u32 s75, s53, 0
	s_add_i32 s69, s67, s56
	global_load_lds_dwordx4 v[218:219], off
	v_lshl_add_u64 v[220:221], s[74:75], 0, v[132:133]
	s_mov_b32 m0, s69
	v_lshl_add_u64 v[222:223], s[54:55], 0, v[134:135]
	global_load_lds_dwordx4 v[220:221], off
	v_lshl_add_u64 v[220:221], s[74:75], 0, v[136:137]
	s_add_i32 m0, s69, 0x2000
	s_nop 0
	global_load_lds_dwordx4 v[220:221], off
	v_lshl_add_u64 v[220:221], s[54:55], 0, v[130:131]
	s_mov_b32 m0, s57
	s_nop 0
	global_load_lds_dwordx4 v[220:221], off
	s_mov_b32 m0, s58
	s_nop 0
	global_load_lds_dwordx4 v[222:223], off
	s_waitcnt vmcnt(8) lgkmcnt(0)
	s_barrier
; #define PG8_LDA(dst, b, h) do { _Pragma("unroll") for (int m = 0; m < 4; ++m) _Pragma("unroll") for (int k = 0; k < 2; ++k) dst[m][k] = *(const PG8_LAS bf16x8*)(lds + PG8_SA(b, h) + aoff + m * 2048 + k * 1024); } while (0)
; #define PG8_LDB(dst, b, h) do { _Pragma("unroll") for (int n = 0; n < 2; ++n) _Pragma("unroll") for (int k = 0; k < 2; ++k) dst[n][k] = *(const PG8_LAS bf16x8*)(lds + PG8_SB(b, h) + boff + n * 2048 + k * 1024); } while (0)
; #define PG8_MMA(ai, bj, At, Bt) do { __builtin_amdgcn_s_setprio(1); _Pragma("unroll") for (int m = 0; m < 4; ++m) _Pragma("unroll") for (int n = 0; n < 2; ++n) _Pragma("unroll") for (int k = 0; k < 2; ++k) \
;         acc[ai][bj][m][n] = __builtin_amdgcn_mfma_f32_16x16x32_bf16(Bt[n][k], At[m][k], acc[ai][bj][m][n], 0, 0, 0); __builtin_amdgcn_s_setprio(0); } while (0)
; #define PG8_WAIT_V(n) asm volatile("s_waitcnt vmcnt(" #n ")" ::: "memory")
; #define PG8_WAIT_L(n) asm volatile("s_waitcnt lgkmcnt(" #n ")" ::: "memory")
; #define PG8_BAR __builtin_amdgcn_s_barrier()
; #define PG8_SCHED __builtin_amdgcn_sched_barrier(0)
; template <class Epi, class Sched, bool ALIGN_EPI = false, bool SP2 = false>
; __device__ __forceinline__ void gemm_phase(PG8_LAS unsigned char* lds, const Gemm g, const Sched& S, const Epi& E) {
;     ...
;             PG8_WAIT_V(8); PG8_WAIT_L(0); PG8_BAR; PG8_MMA(1, 0, At, B0); PG8_MMA(1, 1, At, B1); PG8_BAR; PG8_SCHED;
;             PG8_LDB(B0, 1, 0); PG8_LDB(B1, 1, 1); PG8_SCHED; PG8_LDA(At, 1, 0); PG8_STAGEA(PG8_SA(0, 1), a2, 1, last);
;             PG8_WAIT_V(8); PG8_WAIT_L(0); PG8_BAR; PG8_MMA(0, 0, At, B0); PG8_MMA(0, 1, At, B1); PG8_BAR; PG8_SCHED;
	s_setprio 1
	v_mfma_f32_16x16x32_bf16 v[62:65], v[146:149], v[182:185], v[62:65]
	v_mfma_f32_16x16x32_bf16 v[58:61], v[158:161], v[182:185], v[58:61]
	v_mfma_f32_16x16x32_bf16 v[46:49], v[146:149], v[190:193], v[46:49]
	v_mfma_f32_16x16x32_bf16 v[42:45], v[158:161], v[190:193], v[42:45]
	v_mfma_f32_16x16x32_bf16 v[30:33], v[146:149], v[198:201], v[30:33]
	v_mfma_f32_16x16x32_bf16 v[26:29], v[158:161], v[198:201], v[26:29]
	v_mfma_f32_16x16x32_bf16 v[14:17], v[146:149], v[208:211], v[14:17]
	v_mfma_f32_16x16x32_bf16 v[10:13], v[158:161], v[208:211], v[10:13]
	v_mfma_f32_16x16x32_bf16 v[62:65], v[154:157], v[186:189], v[62:65]
	v_mfma_f32_16x16x32_bf16 v[58:61], v[162:165], v[186:189], v[58:61]
	v_mfma_f32_16x16x32_bf16 v[46:49], v[154:157], v[194:197], v[46:49]
	v_mfma_f32_16x16x32_bf16 v[42:45], v[162:165], v[194:197], v[42:45]
	v_mfma_f32_16x16x32_bf16 v[30:33], v[154:157], v[204:207], v[30:33]
	v_mfma_f32_16x16x32_bf16 v[26:29], v[162:165], v[204:207], v[26:29]
	v_mfma_f32_16x16x32_bf16 v[14:17], v[154:157], v[212:215], v[14:17]
	v_mfma_f32_16x16x32_bf16 v[10:13], v[162:165], v[212:215], v[10:13]
	v_mfma_f32_16x16x32_bf16 v[54:57], v[166:169], v[182:185], v[54:57]
	v_mfma_f32_16x16x32_bf16 v[50:53], v[174:177], v[182:185], v[50:53]
	v_mfma_f32_16x16x32_bf16 v[38:41], v[166:169], v[190:193], v[38:41]
	v_mfma_f32_16x16x32_bf16 v[34:37], v[174:177], v[190:193], v[34:37]
	v_mfma_f32_16x16x32_bf16 v[22:25], v[166:169], v[198:201], v[22:25]
	v_mfma_f32_16x16x32_bf16 v[18:21], v[174:177], v[198:201], v[18:21]
	v_mfma_f32_16x16x32_bf16 v[6:9], v[166:169], v[208:211], v[6:9]
	v_mfma_f32_16x16x32_bf16 v[2:5], v[174:177], v[208:211], v[2:5]
	v_mfma_f32_16x16x32_bf16 v[54:57], v[170:173], v[186:189], v[54:57]
	v_mfma_f32_16x16x32_bf16 v[50:53], v[178:181], v[186:189], v[50:53]
	v_mfma_f32_16x16x32_bf16 v[38:41], v[170:173], v[194:197], v[38:41]
	v_mfma_f32_16x16x32_bf16 v[34:37], v[178:181], v[194:197], v[34:37]
	v_mfma_f32_16x16x32_bf16 v[22:25], v[170:173], v[204:207], v[22:25]
	v_mfma_f32_16x16x32_bf16 v[18:21], v[178:181], v[204:207], v[18:21]
	v_mfma_f32_16x16x32_bf16 v[6:9], v[170:173], v[212:215], v[6:9]
	v_mfma_f32_16x16x32_bf16 v[2:5], v[178:181], v[212:215], v[2:5]
	s_setprio 0
	s_barrier
	s_nop 0
	s_add_i32 s69, 0, 0x18000
	s_add_i32 s74, 0, 0x1c000
	v_add_u32_e32 v162, s69, v150
	v_add_u32_e32 v178, s74, v150
	ds_read_b128 v[146:149], v162
	ds_read_b128 v[154:157], v162 offset:1024
	ds_read_b128 v[158:161], v162 offset:2048
	ds_read_b128 v[162:165], v162 offset:3072
	ds_read_b128 v[166:169], v178
	ds_read_b128 v[170:173], v178 offset:1024
	ds_read_b128 v[174:177], v178 offset:2048
	ds_read_b128 v[178:181], v178 offset:3072
	s_add_u32 s54, s54, 0x80000
	s_addc_u32 s55, s55, 0
	s_mov_b32 m0, s59
	v_lshl_add_u64 v[224:225], s[54:55], 0, v[130:131]
	ds_read_b128 v[182:185], v152 offset:32768
	ds_read_b128 v[186:189], v152 offset:33792
	ds_read_b128 v[190:193], v152 offset:34816
	ds_read_b128 v[194:197], v152 offset:35840
	ds_read_b128 v[198:201], v152 offset:36864
	ds_read_b128 v[204:207], v152 offset:37888
	ds_read_b128 v[208:211], v152 offset:38912
	ds_read_b128 v[212:215], v152 offset:39936
	global_load_lds_dwordx4 v[224:225], off
	v_lshl_add_u64 v[224:225], s[54:55], 0, v[134:135]
	s_mov_b32 m0, s60
	s_nop 0
	global_load_lds_dwordx4 v[224:225], off
	s_waitcnt vmcnt(8) lgkmcnt(0)
	s_barrier
	s_setprio 1
	v_mfma_f32_16x16x32_bf16 v[126:129], v[146:149], v[182:185], v[126:129]
	v_mfma_f32_16x16x32_bf16 v[122:125], v[158:161], v[182:185], v[122:125]
	v_mfma_f32_16x16x32_bf16 v[110:113], v[146:149], v[190:193], v[110:113]
	v_mfma_f32_16x16x32_bf16 v[106:109], v[158:161], v[190:193], v[106:109]
	v_mfma_f32_16x16x32_bf16 v[94:97], v[146:149], v[198:201], v[94:97]
	v_mfma_f32_16x16x32_bf16 v[90:93], v[158:161], v[198:201], v[90:93]
	v_mfma_f32_16x16x32_bf16 v[78:81], v[146:149], v[208:211], v[78:81]
	v_mfma_f32_16x16x32_bf16 v[74:77], v[158:161], v[208:211], v[74:77]
	v_mfma_f32_16x16x32_bf16 v[126:129], v[154:157], v[186:189], v[126:129]
	v_mfma_f32_16x16x32_bf16 v[122:125], v[162:165], v[186:189], v[122:125]
	v_mfma_f32_16x16x32_bf16 v[110:113], v[154:157], v[194:197], v[110:113]
	v_mfma_f32_16x16x32_bf16 v[106:109], v[162:165], v[194:197], v[106:109]
	v_mfma_f32_16x16x32_bf16 v[94:97], v[154:157], v[204:207], v[94:97]
	v_mfma_f32_16x16x32_bf16 v[90:93], v[162:165], v[204:207], v[90:93]
	v_mfma_f32_16x16x32_bf16 v[78:81], v[154:157], v[212:215], v[78:81]
	v_mfma_f32_16x16x32_bf16 v[74:77], v[162:165], v[212:215], v[74:77]
	v_mfma_f32_16x16x32_bf16 v[118:121], v[166:169], v[182:185], v[118:121]
	v_mfma_f32_16x16x32_bf16 v[114:117], v[174:177], v[182:185], v[114:117]
	v_mfma_f32_16x16x32_bf16 v[102:105], v[166:169], v[190:193], v[102:105]
	v_mfma_f32_16x16x32_bf16 v[98:101], v[174:177], v[190:193], v[98:101]
	v_mfma_f32_16x16x32_bf16 v[86:89], v[166:169], v[198:201], v[86:89]
	v_mfma_f32_16x16x32_bf16 v[82:85], v[174:177], v[198:201], v[82:85]
	v_mfma_f32_16x16x32_bf16 v[70:73], v[166:169], v[208:211], v[70:73]
	v_mfma_f32_16x16x32_bf16 v[66:69], v[174:177], v[208:211], v[66:69]
	v_mfma_f32_16x16x32_bf16 v[118:121], v[170:173], v[186:189], v[118:121]
	v_mfma_f32_16x16x32_bf16 v[114:117], v[178:181], v[186:189], v[114:117]
	v_mfma_f32_16x16x32_bf16 v[102:105], v[170:173], v[194:197], v[102:105]
	v_mfma_f32_16x16x32_bf16 v[98:101], v[178:181], v[194:197], v[98:101]
	v_mfma_f32_16x16x32_bf16 v[86:89], v[170:173], v[204:207], v[86:89]
	v_mfma_f32_16x16x32_bf16 v[82:85], v[178:181], v[204:207], v[82:85]
	v_mfma_f32_16x16x32_bf16 v[70:73], v[170:173], v[212:215], v[70:73]
	v_mfma_f32_16x16x32_bf16 v[66:69], v[178:181], v[212:215], v[66:69]
	s_setprio 0
	s_barrier
; #define PG8_STAGE(bufoff, gbase, voff) do { _Pragma("unroll") for (int _i = 0; _i < 2; ++_i) \
;         __builtin_amdgcn_global_load_lds((const unsigned*)((const char*)(gbase) + (voff)[_i]), (PG8_LAS unsigned*)(lds + (bufoff) + ldsw + _i * 8192), 16, 0, 0); } while (0)
; #define PG8_LDA(dst, b, h) do { _Pragma("unroll") for (int m = 0; m < 4; ++m) _Pragma("unroll") for (int k = 0; k < 2; ++k) dst[m][k] = *(const PG8_LAS bf16x8*)(lds + PG8_SA(b, h) + aoff + m * 2048 + k * 1024); } while (0)
; #define PG8_MMA(ai, bj, At, Bt) do { __builtin_amdgcn_s_setprio(1); _Pragma("unroll") for (int m = 0; m < 4; ++m) _Pragma("unroll") for (int n = 0; n < 2; ++n) _Pragma("unroll") for (int k = 0; k < 2; ++k) \
;         acc[ai][bj][m][n] = __builtin_amdgcn_mfma_f32_16x16x32_bf16(Bt[n][k], At[m][k], acc[ai][bj][m][n], 0, 0, 0); __builtin_amdgcn_s_setprio(0); } while (0)
; #define PG8_WAIT_V(n) asm volatile("s_waitcnt vmcnt(" #n ")" ::: "memory")
; #define PG8_WAIT_L(n) asm volatile("s_waitcnt lgkmcnt(" #n ")" ::: "memory")
; #define PG8_BAR __builtin_amdgcn_s_barrier()
; #define PG8_SCHED __builtin_amdgcn_sched_barrier(0)
; template <class Epi, class Sched, bool ALIGN_EPI = false, bool SP2 = false>
; __device__ __forceinline__ void gemm_phase(PG8_LAS unsigned char* lds, const Gemm g, const Sched& S, const Epi& E) {
;     ...
;         for (; t < tend; t += 2) {
;             const bool last = (t == nt - 2);
;             const char* a1 = cA + (size_t)(t + 1) * kstep;
;             const char* a2 = last ? nA : cA + (size_t)(t + 2) * kstep; const char* b2 = last ? nB : cB + (size_t)(t + 2) * kstep;
;     ...
;             PG8_LDA(At, 1, 1); PG8_STAGE(PG8_SB(1, 0), b3, voffB); PG8_STAGE(PG8_SB(1, 1), b3 + hstep, voffB); PG8_STAGEA(PG8_SA(1, 0), a3, 0, last);
;             PG8_WAIT_V(8); PG8_WAIT_L(0); PG8_BAR; PG8_MMA(1, 0, At, B0); PG8_MMA(1, 1, At, B1); PG8_BAR; PG8_SCHED;
	s_add_i32 s54, s69, s56
	v_lshl_add_u64 v[216:217], v[216:217], 0, s[26:27]
	s_mov_b32 m0, s54
	ds_read_b128 v[182:185], v152 offset:49152
	ds_read_b128 v[186:189], v152 offset:50176
	ds_read_b128 v[190:193], v152 offset:51200
	ds_read_b128 v[194:197], v152 offset:52224
	ds_read_b128 v[198:201], v152 offset:53248
	ds_read_b128 v[204:207], v152 offset:54272
	ds_read_b128 v[208:211], v152 offset:55296
	ds_read_b128 v[212:215], v152 offset:56320
	global_load_lds_dwordx4 v[216:217], off
	s_add_i32 m0, s54, 0x2000
	s_add_u32 s52, s52, 0x80080
	v_lshl_add_u64 v[216:217], v[218:219], 0, s[26:27]
	s_addc_u32 s53, s53, 0
	s_add_i32 s54, s74, s56
	global_load_lds_dwordx4 v[216:217], off
	v_lshl_add_u64 v[216:217], s[52:53], 0, v[132:133]
	s_mov_b32 m0, s54
	s_nop 0
	global_load_lds_dwordx4 v[216:217], off
	v_lshl_add_u64 v[216:217], s[52:53], 0, v[136:137]
	s_add_i32 m0, s54, 0x2000
	s_nop 0
	global_load_lds_dwordx4 v[216:217], off
	v_lshl_add_u64 v[216:217], v[220:221], 0, s[26:27]
	s_mov_b32 m0, s62
	s_nop 0
	global_load_lds_dwordx4 v[216:217], off
	v_lshl_add_u64 v[216:217], v[222:223], 0, s[26:27]
	s_mov_b32 m0, s63
	s_nop 0
	global_load_lds_dwordx4 v[216:217], off
	s_waitcnt vmcnt(8) lgkmcnt(0)
	s_barrier
	s_setprio 1
	v_mfma_f32_16x16x32_bf16 v[62:65], v[146:149], v[182:185], v[62:65]
	v_mfma_f32_16x16x32_bf16 v[58:61], v[158:161], v[182:185], v[58:61]
	v_mfma_f32_16x16x32_bf16 v[46:49], v[146:149], v[190:193], v[46:49]
	v_mfma_f32_16x16x32_bf16 v[42:45], v[158:161], v[190:193], v[42:45]
	v_mfma_f32_16x16x32_bf16 v[30:33], v[146:149], v[198:201], v[30:33]
	v_mfma_f32_16x16x32_bf16 v[26:29], v[158:161], v[198:201], v[26:29]
	v_mfma_f32_16x16x32_bf16 v[14:17], v[146:149], v[208:211], v[14:17]
	v_mfma_f32_16x16x32_bf16 v[10:13], v[158:161], v[208:211], v[10:13]
	v_mfma_f32_16x16x32_bf16 v[62:65], v[154:157], v[186:189], v[62:65]
	v_mfma_f32_16x16x32_bf16 v[58:61], v[162:165], v[186:189], v[58:61]
	v_mfma_f32_16x16x32_bf16 v[46:49], v[154:157], v[194:197], v[46:49]
	v_mfma_f32_16x16x32_bf16 v[42:45], v[162:165], v[194:197], v[42:45]
	v_mfma_f32_16x16x32_bf16 v[30:33], v[154:157], v[204:207], v[30:33]
	v_mfma_f32_16x16x32_bf16 v[26:29], v[162:165], v[204:207], v[26:29]
	v_mfma_f32_16x16x32_bf16 v[14:17], v[154:157], v[212:215], v[14:17]
	v_mfma_f32_16x16x32_bf16 v[10:13], v[162:165], v[212:215], v[10:13]
	v_mfma_f32_16x16x32_bf16 v[54:57], v[166:169], v[182:185], v[54:57]
	v_mfma_f32_16x16x32_bf16 v[50:53], v[174:177], v[182:185], v[50:53]
	v_mfma_f32_16x16x32_bf16 v[38:41], v[166:169], v[190:193], v[38:41]
	v_mfma_f32_16x16x32_bf16 v[34:37], v[174:177], v[190:193], v[34:37]
	v_mfma_f32_16x16x32_bf16 v[22:25], v[166:169], v[198:201], v[22:25]
	v_mfma_f32_16x16x32_bf16 v[18:21], v[174:177], v[198:201], v[18:21]
	v_mfma_f32_16x16x32_bf16 v[6:9], v[166:169], v[208:211], v[6:9]
	v_mfma_f32_16x16x32_bf16 v[2:5], v[174:177], v[208:211], v[2:5]
	v_mfma_f32_16x16x32_bf16 v[54:57], v[170:173], v[186:189], v[54:57]
	v_mfma_f32_16x16x32_bf16 v[50:53], v[178:181], v[186:189], v[50:53]
	v_mfma_f32_16x16x32_bf16 v[38:41], v[170:173], v[194:197], v[38:41]
	v_mfma_f32_16x16x32_bf16 v[34:37], v[178:181], v[194:197], v[34:37]
	v_mfma_f32_16x16x32_bf16 v[22:25], v[170:173], v[204:207], v[22:25]
	v_mfma_f32_16x16x32_bf16 v[18:21], v[178:181], v[204:207], v[18:21]
	v_mfma_f32_16x16x32_bf16 v[6:9], v[170:173], v[212:215], v[6:9]
	v_mfma_f32_16x16x32_bf16 v[2:5], v[178:181], v[212:215], v[2:5]
	s_setprio 0
	s_barrier
	s_add_i32 s49, s49, 2
	s_add_u32 s50, s50, 0x100
	s_addc_u32 s51, s51, 0
	s_add_u32 s41, s41, 0x100
	s_addc_u32 s43, s43, 0
	s_cmp_gt_u32 s49, 29
	s_cbranch_scc0 .LBB0_571
	s_nop 0
	s_and_b64 vcc, exec, s[38:39]
	s_cbranch_vccz .LBB0_574
	s_barrier

; #define PG8_STAGE(bufoff, gbase, voff) do { _Pragma("unroll") for (int _i = 0; _i < 2; ++_i) \
;         __builtin_amdgcn_global_load_lds((const unsigned*)((const char*)(gbase) + (voff)[_i]), (PG8_LAS unsigned*)(lds + (bufoff) + ldsw + _i * 8192), 16, 0, 0); } while (0)
; #define PG8_LDA(dst, b, h) do { _Pragma("unroll") for (int m = 0; m < 4; ++m) _Pragma("unroll") for (int k = 0; k < 2; ++k) dst[m][k] = *(const PG8_LAS bf16x8*)(lds + PG8_SA(b, h) + aoff + m * 2048 + k * 1024); } while (0)
; #define PG8_LDB(dst, b, h) do { _Pragma("unroll") for (int n = 0; n < 2; ++n) _Pragma("unroll") for (int k = 0; k < 2; ++k) dst[n][k] = *(const PG8_LAS bf16x8*)(lds + PG8_SB(b, h) + boff + n * 2048 + k * 1024); } while (0)
; #define PG8_MMA(ai, bj, At, Bt) do { __builtin_amdgcn_s_setprio(1); _Pragma("unroll") for (int m = 0; m < 4; ++m) _Pragma("unroll") for (int n = 0; n < 2; ++n) _Pragma("unroll") for (int k = 0; k < 2; ++k) \
;         acc[ai][bj][m][n] = __builtin_amdgcn_mfma_f32_16x16x32_bf16(Bt[n][k], At[m][k], acc[ai][bj][m][n], 0, 0, 0); __builtin_amdgcn_s_setprio(0); } while (0)
; #define PG8_WAIT_V(n) asm volatile("s_waitcnt vmcnt(" #n ")" ::: "memory")
; #define PG8_WAIT_L(n) asm volatile("s_waitcnt lgkmcnt(" #n ")" ::: "memory")
; #define PG8_BAR __builtin_amdgcn_s_barrier()
; #define PG8_SCHED __builtin_amdgcn_sched_barrier(0)
; template <class Epi, class Sched, bool ALIGN_EPI = false, bool SP2 = false>
; __device__ __forceinline__ void gemm_phase(PG8_LAS unsigned char* lds, const Gemm g, const Sched& S, const Epi& E) {
;     ...
;             const bool last = (t == nt - 2);
;             const char* a1 = cA + (size_t)(t + 1) * kstep;
;             const char* a2 = last ? nA : cA + (size_t)(t + 2) * kstep; const char* b2 = last ? nB : cB + (size_t)(t + 2) * kstep;
;             const char* a3 = a2 + kstep; const char* b3 = b2 + kstep;
;             if (last && has_next) S.a_ready(nxt);
;             if constexpr (SP2) {
;             PG8_LDB(B0, 0, 0); PG8_LDB(B1, 0, 1); PG8_SCHED; PG8_LDA(At, 0, 0); PG8_STAGEA(PG8_SA(1, 1), a1, 1, false);
;             PG8_WAIT_V(8); PG8_WAIT_L(0); PG8_BAR; PG8_MMA(0, 0, At, B0); PG8_MMA(0, 1, At, B1); PG8_BAR; PG8_SCHED;
;             PG8_LDA(At, 0, 1); PG8_STAGE(PG8_SB(0, 0), b2, voffB); PG8_STAGE(PG8_SB(0, 1), b2 + hstep, voffB); PG8_STAGEA(PG8_SA(0, 0), a2, 0, last);
.LBB0_792:
	s_nop 0
	s_add_u32 s6, s12, 0x100
	v_add_u32_e32 v134, s84, v152
	s_addc_u32 s7, s13, 0
	ds_read_b128 v[162:165], v134
	ds_read_b128 v[166:169], v134 offset:1024
	ds_read_b128 v[170:173], v134 offset:2048
	ds_read_b128 v[174:177], v134 offset:3072
	v_add_u32_e32 v134, s85, v152
	s_add_u32 s10, s16, s12
	ds_read_b128 v[178:181], v134
	ds_read_b128 v[182:185], v134 offset:1024
	ds_read_b128 v[186:189], v134 offset:2048
	ds_read_b128 v[190:193], v134 offset:3072
	s_addc_u32 s11, s17, s13
	s_cmpk_eq_i32 s12, 0xf00
	s_cselect_b64 vcc, -1, 0
	s_and_b64 s[8:9], vcc, exec
	s_cselect_b32 s36, 0, s6
	s_cselect_b32 s27, 0, s7
	s_cselect_b32 s8, s18, s10
	s_cselect_b32 s9, s15, s11
	s_add_u32 s10, s42, s36
	s_addc_u32 s11, s43, s27
	v_lshl_add_u64 v[228:229], v[142:143], 0, s[12:13]
	s_add_i32 m0, s77, 0xc000
	ds_read_b128 v[194:197], v156
	ds_read_b128 v[198:201], v156 offset:1024
	ds_read_b128 v[204:207], v156 offset:2048
	ds_read_b128 v[208:211], v156 offset:3072
	ds_read_b128 v[212:215], v156 offset:4096
	ds_read_b128 v[216:219], v156 offset:5120
	ds_read_b128 v[220:223], v156 offset:6144
	ds_read_b128 v[224:227], v156 offset:7168
	global_load_lds_dwordx4 v[228:229], off
	v_lshl_add_u64 v[228:229], v[144:145], 0, s[12:13]
	s_add_i32 m0, s77, 0xe000
	s_nop 0
	global_load_lds_dwordx4 v[228:229], off
	s_waitcnt vmcnt(8) lgkmcnt(0)
	s_barrier
	s_setprio 1
	v_mfma_f32_16x16x32_bf16 v[126:129], v[162:165], v[194:197], v[126:129]
	v_mfma_f32_16x16x32_bf16 v[118:121], v[170:173], v[194:197], v[118:121]
	v_mfma_f32_16x16x32_bf16 v[110:113], v[162:165], v[204:207], v[110:113]
	v_mfma_f32_16x16x32_bf16 v[102:105], v[170:173], v[204:207], v[102:105]
	v_mfma_f32_16x16x32_bf16 v[94:97], v[162:165], v[212:215], v[94:97]
	v_mfma_f32_16x16x32_bf16 v[86:89], v[170:173], v[212:215], v[86:89]
	v_mfma_f32_16x16x32_bf16 v[78:81], v[162:165], v[220:223], v[78:81]
	v_mfma_f32_16x16x32_bf16 v[70:73], v[170:173], v[220:223], v[70:73]
	v_mfma_f32_16x16x32_bf16 v[126:129], v[166:169], v[198:201], v[126:129]
	v_mfma_f32_16x16x32_bf16 v[118:121], v[174:177], v[198:201], v[118:121]
	v_mfma_f32_16x16x32_bf16 v[110:113], v[166:169], v[208:211], v[110:113]
	v_mfma_f32_16x16x32_bf16 v[102:105], v[174:177], v[208:211], v[102:105]
	v_mfma_f32_16x16x32_bf16 v[94:97], v[166:169], v[216:219], v[94:97]
	v_mfma_f32_16x16x32_bf16 v[86:89], v[174:177], v[216:219], v[86:89]
	v_mfma_f32_16x16x32_bf16 v[78:81], v[166:169], v[224:227], v[78:81]
	v_mfma_f32_16x16x32_bf16 v[70:73], v[174:177], v[224:227], v[70:73]
	v_mfma_f32_16x16x32_bf16 v[122:125], v[178:181], v[194:197], v[122:125]
	v_mfma_f32_16x16x32_bf16 v[114:117], v[186:189], v[194:197], v[114:117]
	v_mfma_f32_16x16x32_bf16 v[106:109], v[178:181], v[204:207], v[106:109]
	v_mfma_f32_16x16x32_bf16 v[98:101], v[186:189], v[204:207], v[98:101]
	v_mfma_f32_16x16x32_bf16 v[90:93], v[178:181], v[212:215], v[90:93]
	v_mfma_f32_16x16x32_bf16 v[82:85], v[186:189], v[212:215], v[82:85]
	v_mfma_f32_16x16x32_bf16 v[74:77], v[178:181], v[220:223], v[74:77]
	v_mfma_f32_16x16x32_bf16 v[66:69], v[186:189], v[220:223], v[66:69]
	v_mfma_f32_16x16x32_bf16 v[122:125], v[182:185], v[198:201], v[122:125]
	v_mfma_f32_16x16x32_bf16 v[114:117], v[190:193], v[198:201], v[114:117]
	v_mfma_f32_16x16x32_bf16 v[106:109], v[182:185], v[208:211], v[106:109]
	v_mfma_f32_16x16x32_bf16 v[98:101], v[190:193], v[208:211], v[98:101]
	v_mfma_f32_16x16x32_bf16 v[90:93], v[182:185], v[216:219], v[90:93]
	v_mfma_f32_16x16x32_bf16 v[82:85], v[190:193], v[216:219], v[82:85]
	v_mfma_f32_16x16x32_bf16 v[74:77], v[182:185], v[224:227], v[74:77]
	v_mfma_f32_16x16x32_bf16 v[66:69], v[190:193], v[224:227], v[66:69]
	s_setprio 0
	s_barrier
	s_nop 0
	s_add_i32 s12, s84, s76
	v_lshl_add_u64 v[228:229], s[8:9], 0, v[130:131]
	s_mov_b32 m0, s12
	ds_read_b128 v[194:197], v156 offset:16384
	ds_read_b128 v[198:201], v156 offset:17408
	ds_read_b128 v[204:207], v156 offset:18432
	ds_read_b128 v[208:211], v156 offset:19456
	ds_read_b128 v[212:215], v156 offset:20480
	ds_read_b128 v[216:219], v156 offset:21504
	ds_read_b128 v[220:223], v156 offset:22528
	ds_read_b128 v[224:227], v156 offset:23552
	global_load_lds_dwordx4 v[228:229], off
	s_add_i32 m0, s12, 0x2000
	s_add_u32 s12, s8, 0x80000
	v_lshl_add_u64 v[230:231], s[8:9], 0, v[132:133]
	s_addc_u32 s13, s9, 0
	s_add_i32 s27, s85, s76
	global_load_lds_dwordx4 v[230:231], off
	v_lshl_add_u64 v[232:233], s[12:13], 0, v[130:131]
	s_mov_b32 m0, s27
	v_cndmask_b32_e32 v134, v146, v157, vcc
	global_load_lds_dwordx4 v[232:233], off
	v_lshl_add_u64 v[232:233], s[12:13], 0, v[132:133]
	s_add_i32 m0, s27, 0x2000
	s_nop 0
	global_load_lds_dwordx4 v[232:233], off
	s_mov_b32 m0, s77
	v_lshl_add_u64 v[232:233], s[10:11], 0, v[134:135]
	global_load_lds_dwordx4 v134, s[10:11]
	v_cndmask_b32_e32 v134, v136, v158, vcc
	s_mov_b32 m0, s78
	v_lshl_add_u64 v[234:235], s[10:11], 0, v[134:135]
	global_load_lds_dwordx4 v134, s[10:11]
	s_waitcnt vmcnt(8) lgkmcnt(0)
	s_barrier
; #define PG8_LDA(dst, b, h) do { _Pragma("unroll") for (int m = 0; m < 4; ++m) _Pragma("unroll") for (int k = 0; k < 2; ++k) dst[m][k] = *(const PG8_LAS bf16x8*)(lds + PG8_SA(b, h) + aoff + m * 2048 + k * 1024); } while (0)
; #define PG8_LDB(dst, b, h) do { _Pragma("unroll") for (int n = 0; n < 2; ++n) _Pragma("unroll") for (int k = 0; k < 2; ++k) dst[n][k] = *(const PG8_LAS bf16x8*)(lds + PG8_SB(b, h) + boff + n * 2048 + k * 1024); } while (0)
; #define PG8_MMA(ai, bj, At, Bt) do { __builtin_amdgcn_s_setprio(1); _Pragma("unroll") for (int m = 0; m < 4; ++m) _Pragma("unroll") for (int n = 0; n < 2; ++n) _Pragma("unroll") for (int k = 0; k < 2; ++k) \
;         acc[ai][bj][m][n] = __builtin_amdgcn_mfma_f32_16x16x32_bf16(Bt[n][k], At[m][k], acc[ai][bj][m][n], 0, 0, 0); __builtin_amdgcn_s_setprio(0); } while (0)
; #define PG8_WAIT_V(n) asm volatile("s_waitcnt vmcnt(" #n ")" ::: "memory")
; #define PG8_WAIT_L(n) asm volatile("s_waitcnt lgkmcnt(" #n ")" ::: "memory")
; #define PG8_BAR __builtin_amdgcn_s_barrier()
; #define PG8_SCHED __builtin_amdgcn_sched_barrier(0)
; template <class Epi, class Sched, bool ALIGN_EPI = false, bool SP2 = false>
; __device__ __forceinline__ void gemm_phase(PG8_LAS unsigned char* lds, const Gemm g, const Sched& S, const Epi& E) {
;     ...
;             PG8_WAIT_V(8); PG8_WAIT_L(0); PG8_BAR; PG8_MMA(1, 0, At, B0); PG8_MMA(1, 1, At, B1); PG8_BAR; PG8_SCHED;
;             PG8_LDB(B0, 1, 0); PG8_LDB(B1, 1, 1); PG8_SCHED; PG8_LDA(At, 1, 0); PG8_STAGEA(PG8_SA(0, 1), a2, 1, last);
;             PG8_WAIT_V(8); PG8_WAIT_L(0); PG8_BAR; PG8_MMA(0, 0, At, B0); PG8_MMA(0, 1, At, B1); PG8_BAR; PG8_SCHED;
	s_setprio 1
	v_mfma_f32_16x16x32_bf16 v[62:65], v[162:165], v[194:197], v[62:65]
	v_mfma_f32_16x16x32_bf16 v[54:57], v[170:173], v[194:197], v[54:57]
	v_mfma_f32_16x16x32_bf16 v[46:49], v[162:165], v[204:207], v[46:49]
	v_mfma_f32_16x16x32_bf16 v[38:41], v[170:173], v[204:207], v[38:41]
	v_mfma_f32_16x16x32_bf16 v[30:33], v[162:165], v[212:215], v[30:33]
	v_mfma_f32_16x16x32_bf16 v[22:25], v[170:173], v[212:215], v[22:25]
	v_mfma_f32_16x16x32_bf16 v[14:17], v[162:165], v[220:223], v[14:17]
	v_mfma_f32_16x16x32_bf16 v[6:9], v[170:173], v[220:223], v[6:9]
	v_mfma_f32_16x16x32_bf16 v[62:65], v[166:169], v[198:201], v[62:65]
	v_mfma_f32_16x16x32_bf16 v[54:57], v[174:177], v[198:201], v[54:57]
	v_mfma_f32_16x16x32_bf16 v[46:49], v[166:169], v[208:211], v[46:49]
	v_mfma_f32_16x16x32_bf16 v[38:41], v[174:177], v[208:211], v[38:41]
	v_mfma_f32_16x16x32_bf16 v[30:33], v[166:169], v[216:219], v[30:33]
	v_mfma_f32_16x16x32_bf16 v[22:25], v[174:177], v[216:219], v[22:25]
	v_mfma_f32_16x16x32_bf16 v[14:17], v[166:169], v[224:227], v[14:17]
	v_mfma_f32_16x16x32_bf16 v[6:9], v[174:177], v[224:227], v[6:9]
	v_mfma_f32_16x16x32_bf16 v[58:61], v[178:181], v[194:197], v[58:61]
	v_mfma_f32_16x16x32_bf16 v[50:53], v[186:189], v[194:197], v[50:53]
	v_mfma_f32_16x16x32_bf16 v[42:45], v[178:181], v[204:207], v[42:45]
	v_mfma_f32_16x16x32_bf16 v[34:37], v[186:189], v[204:207], v[34:37]
	v_mfma_f32_16x16x32_bf16 v[26:29], v[178:181], v[212:215], v[26:29]
	v_mfma_f32_16x16x32_bf16 v[18:21], v[186:189], v[212:215], v[18:21]
	v_mfma_f32_16x16x32_bf16 v[10:13], v[178:181], v[220:223], v[10:13]
	v_mfma_f32_16x16x32_bf16 v[2:5], v[186:189], v[220:223], v[2:5]
	v_mfma_f32_16x16x32_bf16 v[58:61], v[182:185], v[198:201], v[58:61]
	v_mfma_f32_16x16x32_bf16 v[50:53], v[190:193], v[198:201], v[50:53]
	v_mfma_f32_16x16x32_bf16 v[42:45], v[182:185], v[208:211], v[42:45]
	v_mfma_f32_16x16x32_bf16 v[34:37], v[190:193], v[208:211], v[34:37]
	v_mfma_f32_16x16x32_bf16 v[26:29], v[182:185], v[216:219], v[26:29]
	v_mfma_f32_16x16x32_bf16 v[18:21], v[190:193], v[216:219], v[18:21]
	v_mfma_f32_16x16x32_bf16 v[10:13], v[182:185], v[224:227], v[10:13]
	v_mfma_f32_16x16x32_bf16 v[2:5], v[190:193], v[224:227], v[2:5]
	s_setprio 0
	s_barrier
	s_add_i32 s12, 0, 0x18000
	v_add_u32_e32 v134, s12, v152
	s_add_i32 s13, 0, 0x1c000
	ds_read_b128 v[162:165], v134
	ds_read_b128 v[166:169], v134 offset:1024
	ds_read_b128 v[170:173], v134 offset:2048
	ds_read_b128 v[174:177], v134 offset:3072
	v_add_u32_e32 v134, s13, v152
	ds_read_b128 v[178:181], v134
	ds_read_b128 v[182:185], v134 offset:1024
	ds_read_b128 v[186:189], v134 offset:2048
	ds_read_b128 v[190:193], v134 offset:3072
	s_mov_b32 m0, s79
	v_cndmask_b32_e32 v134, v138, v159, vcc
	ds_read_b128 v[194:197], v156 offset:32768
	ds_read_b128 v[198:201], v156 offset:33792
	ds_read_b128 v[204:207], v156 offset:34816
	ds_read_b128 v[208:211], v156 offset:35840
	ds_read_b128 v[212:215], v156 offset:36864
	ds_read_b128 v[216:219], v156 offset:37888
	ds_read_b128 v[220:223], v156 offset:38912
	ds_read_b128 v[224:227], v156 offset:39936
	global_load_lds_dwordx4 v134, s[10:11]
	v_cndmask_b32_e32 v134, v140, v160, vcc
	s_mov_b32 m0, s80
	s_nop 0
	global_load_lds_dwordx4 v134, s[10:11]
	s_waitcnt vmcnt(8) lgkmcnt(0)
	s_barrier
	s_setprio 1
	v_mfma_f32_16x16x32_bf16 v[126:129], v[162:165], v[194:197], v[126:129]
	v_mfma_f32_16x16x32_bf16 v[118:121], v[170:173], v[194:197], v[118:121]
	v_mfma_f32_16x16x32_bf16 v[110:113], v[162:165], v[204:207], v[110:113]
	v_mfma_f32_16x16x32_bf16 v[102:105], v[170:173], v[204:207], v[102:105]
	v_mfma_f32_16x16x32_bf16 v[94:97], v[162:165], v[212:215], v[94:97]
	v_mfma_f32_16x16x32_bf16 v[86:89], v[170:173], v[212:215], v[86:89]
	v_mfma_f32_16x16x32_bf16 v[78:81], v[162:165], v[220:223], v[78:81]
	v_mfma_f32_16x16x32_bf16 v[70:73], v[170:173], v[220:223], v[70:73]
	v_mfma_f32_16x16x32_bf16 v[126:129], v[166:169], v[198:201], v[126:129]
	v_mfma_f32_16x16x32_bf16 v[118:121], v[174:177], v[198:201], v[118:121]
	v_mfma_f32_16x16x32_bf16 v[110:113], v[166:169], v[208:211], v[110:113]
	v_mfma_f32_16x16x32_bf16 v[102:105], v[174:177], v[208:211], v[102:105]
	v_mfma_f32_16x16x32_bf16 v[94:97], v[166:169], v[216:219], v[94:97]
	v_mfma_f32_16x16x32_bf16 v[86:89], v[174:177], v[216:219], v[86:89]
	v_mfma_f32_16x16x32_bf16 v[78:81], v[166:169], v[224:227], v[78:81]
	v_mfma_f32_16x16x32_bf16 v[70:73], v[174:177], v[224:227], v[70:73]
	v_mfma_f32_16x16x32_bf16 v[122:125], v[178:181], v[194:197], v[122:125]
	v_mfma_f32_16x16x32_bf16 v[114:117], v[186:189], v[194:197], v[114:117]
	v_mfma_f32_16x16x32_bf16 v[106:109], v[178:181], v[204:207], v[106:109]
	v_mfma_f32_16x16x32_bf16 v[98:101], v[186:189], v[204:207], v[98:101]
	v_mfma_f32_16x16x32_bf16 v[90:93], v[178:181], v[212:215], v[90:93]
	v_mfma_f32_16x16x32_bf16 v[82:85], v[186:189], v[212:215], v[82:85]
	v_mfma_f32_16x16x32_bf16 v[74:77], v[178:181], v[220:223], v[74:77]
	v_mfma_f32_16x16x32_bf16 v[66:69], v[186:189], v[220:223], v[66:69]
	v_mfma_f32_16x16x32_bf16 v[122:125], v[182:185], v[198:201], v[122:125]
	v_mfma_f32_16x16x32_bf16 v[114:117], v[190:193], v[198:201], v[114:117]
	v_mfma_f32_16x16x32_bf16 v[106:109], v[182:185], v[208:211], v[106:109]
	v_mfma_f32_16x16x32_bf16 v[98:101], v[190:193], v[208:211], v[98:101]
	v_mfma_f32_16x16x32_bf16 v[90:93], v[182:185], v[216:219], v[90:93]
	v_mfma_f32_16x16x32_bf16 v[82:85], v[190:193], v[216:219], v[82:85]
	v_mfma_f32_16x16x32_bf16 v[74:77], v[182:185], v[224:227], v[74:77]
	v_mfma_f32_16x16x32_bf16 v[66:69], v[190:193], v[224:227], v[66:69]
	s_setprio 0
	s_barrier
; #define PG8_STAGE(bufoff, gbase, voff) do { _Pragma("unroll") for (int _i = 0; _i < 2; ++_i) \
;         __builtin_amdgcn_global_load_lds((const unsigned*)((const char*)(gbase) + (voff)[_i]), (PG8_LAS unsigned*)(lds + (bufoff) + ldsw + _i * 8192), 16, 0, 0); } while (0)
; #define PG8_LDA(dst, b, h) do { _Pragma("unroll") for (int m = 0; m < 4; ++m) _Pragma("unroll") for (int k = 0; k < 2; ++k) dst[m][k] = *(const PG8_LAS bf16x8*)(lds + PG8_SA(b, h) + aoff + m * 2048 + k * 1024); } while (0)
; #define PG8_MMA(ai, bj, At, Bt) do { __builtin_amdgcn_s_setprio(1); _Pragma("unroll") for (int m = 0; m < 4; ++m) _Pragma("unroll") for (int n = 0; n < 2; ++n) _Pragma("unroll") for (int k = 0; k < 2; ++k) \
;         acc[ai][bj][m][n] = __builtin_amdgcn_mfma_f32_16x16x32_bf16(Bt[n][k], At[m][k], acc[ai][bj][m][n], 0, 0, 0); __builtin_amdgcn_s_setprio(0); } while (0)
; #define PG8_WAIT_V(n) asm volatile("s_waitcnt vmcnt(" #n ")" ::: "memory")
; #define PG8_WAIT_L(n) asm volatile("s_waitcnt lgkmcnt(" #n ")" ::: "memory")
; #define PG8_BAR __builtin_amdgcn_s_barrier()
; #define PG8_SCHED __builtin_amdgcn_sched_barrier(0)
; template <class Epi, class Sched, bool ALIGN_EPI = false, bool SP2 = false>
; __device__ __forceinline__ void gemm_phase(PG8_LAS unsigned char* lds, const Gemm g, const Sched& S, const Epi& E) {
;     ...
;         for (; t < tend; t += 2) {
;     ...
;             PG8_LDA(At, 1, 1); PG8_STAGE(PG8_SB(1, 0), b3, voffB); PG8_STAGE(PG8_SB(1, 1), b3 + hstep, voffB); PG8_STAGEA(PG8_SA(1, 0), a3, 0, last);
;             PG8_WAIT_V(8); PG8_WAIT_L(0); PG8_BAR; PG8_MMA(1, 0, At, B0); PG8_MMA(1, 1, At, B1); PG8_BAR; PG8_SCHED;
	s_add_i32 s10, s12, s76
	v_lshl_add_u64 v[228:229], v[228:229], 0, s[52:53]
	s_mov_b32 m0, s10
	ds_read_b128 v[194:197], v156 offset:49152
	ds_read_b128 v[198:201], v156 offset:50176
	ds_read_b128 v[204:207], v156 offset:51200
	ds_read_b128 v[208:211], v156 offset:52224
	ds_read_b128 v[212:215], v156 offset:53248
	ds_read_b128 v[216:219], v156 offset:54272
	ds_read_b128 v[220:223], v156 offset:55296
	ds_read_b128 v[224:227], v156 offset:56320
	global_load_lds_dwordx4 v[228:229], off
	s_add_i32 m0, s10, 0x2000
	s_add_u32 s8, s8, 0x80080
	v_lshl_add_u64 v[228:229], v[230:231], 0, s[52:53]
	s_addc_u32 s9, s9, 0
	s_add_i32 s10, s13, s76
	global_load_lds_dwordx4 v[228:229], off
	v_lshl_add_u64 v[228:229], s[8:9], 0, v[130:131]
	s_mov_b32 m0, s10
	s_nop 0
	global_load_lds_dwordx4 v[228:229], off
	v_lshl_add_u64 v[228:229], s[8:9], 0, v[132:133]
	s_add_i32 m0, s10, 0x2000
	s_nop 0
	global_load_lds_dwordx4 v[228:229], off
	v_lshl_add_u64 v[228:229], v[232:233], 0, s[52:53]
	s_mov_b32 m0, s81
	s_nop 0
	global_load_lds_dwordx4 v[228:229], off
	v_lshl_add_u64 v[228:229], v[234:235], 0, s[52:53]
	s_mov_b32 m0, s82
	s_nop 0
	global_load_lds_dwordx4 v[228:229], off
	s_waitcnt vmcnt(8) lgkmcnt(0)
	s_barrier
	s_setprio 1
	v_mfma_f32_16x16x32_bf16 v[62:65], v[162:165], v[194:197], v[62:65]
	v_mfma_f32_16x16x32_bf16 v[54:57], v[170:173], v[194:197], v[54:57]
	v_mfma_f32_16x16x32_bf16 v[46:49], v[162:165], v[204:207], v[46:49]
	v_mfma_f32_16x16x32_bf16 v[38:41], v[170:173], v[204:207], v[38:41]
	v_mfma_f32_16x16x32_bf16 v[30:33], v[162:165], v[212:215], v[30:33]
	v_mfma_f32_16x16x32_bf16 v[22:25], v[170:173], v[212:215], v[22:25]
	v_mfma_f32_16x16x32_bf16 v[14:17], v[162:165], v[220:223], v[14:17]
	v_mfma_f32_16x16x32_bf16 v[6:9], v[170:173], v[220:223], v[6:9]
	v_mfma_f32_16x16x32_bf16 v[62:65], v[166:169], v[198:201], v[62:65]
	v_mfma_f32_16x16x32_bf16 v[54:57], v[174:177], v[198:201], v[54:57]
	v_mfma_f32_16x16x32_bf16 v[46:49], v[166:169], v[208:211], v[46:49]
	v_mfma_f32_16x16x32_bf16 v[38:41], v[174:177], v[208:211], v[38:41]
	v_mfma_f32_16x16x32_bf16 v[30:33], v[166:169], v[216:219], v[30:33]
	v_mfma_f32_16x16x32_bf16 v[22:25], v[174:177], v[216:219], v[22:25]
	v_mfma_f32_16x16x32_bf16 v[14:17], v[166:169], v[224:227], v[14:17]
	v_mfma_f32_16x16x32_bf16 v[6:9], v[174:177], v[224:227], v[6:9]
	v_mfma_f32_16x16x32_bf16 v[58:61], v[178:181], v[194:197], v[58:61]
	v_mfma_f32_16x16x32_bf16 v[50:53], v[186:189], v[194:197], v[50:53]
	v_mfma_f32_16x16x32_bf16 v[42:45], v[178:181], v[204:207], v[42:45]
	v_mfma_f32_16x16x32_bf16 v[34:37], v[186:189], v[204:207], v[34:37]
	v_mfma_f32_16x16x32_bf16 v[26:29], v[178:181], v[212:215], v[26:29]
	v_mfma_f32_16x16x32_bf16 v[18:21], v[186:189], v[212:215], v[18:21]
	v_mfma_f32_16x16x32_bf16 v[10:13], v[178:181], v[220:223], v[10:13]
	v_mfma_f32_16x16x32_bf16 v[2:5], v[186:189], v[220:223], v[2:5]
	v_mfma_f32_16x16x32_bf16 v[58:61], v[182:185], v[198:201], v[58:61]
	v_mfma_f32_16x16x32_bf16 v[50:53], v[190:193], v[198:201], v[50:53]
	v_mfma_f32_16x16x32_bf16 v[42:45], v[182:185], v[208:211], v[42:45]
	v_mfma_f32_16x16x32_bf16 v[34:37], v[190:193], v[208:211], v[34:37]
	v_mfma_f32_16x16x32_bf16 v[26:29], v[182:185], v[216:219], v[26:29]
	v_mfma_f32_16x16x32_bf16 v[18:21], v[190:193], v[216:219], v[18:21]
	v_mfma_f32_16x16x32_bf16 v[10:13], v[182:185], v[224:227], v[10:13]
	v_mfma_f32_16x16x32_bf16 v[2:5], v[190:193], v[224:227], v[2:5]
	s_setprio 0
	s_barrier
	s_add_i32 s19, s19, 2
	s_cmp_gt_u32 s19, 29
	s_mov_b64 s[12:13], s[6:7]
	s_cbranch_scc0 .LBB0_792
	s_and_b64 vcc, exec, s[56:57]
	s_cbranch_vccz .LBB0_795
	s_barrier

; #define PG8_STAGE(bufoff, gbase, voff) do { _Pragma("unroll") for (int _i = 0; _i < 2; ++_i) \
;         __builtin_amdgcn_global_load_lds((const unsigned*)((const char*)(gbase) + (voff)[_i]), (PG8_LAS unsigned*)(lds + (bufoff) + ldsw + _i * 8192), 16, 0, 0); } while (0)
; #define PG8_LDA(dst, b, h) do { _Pragma("unroll") for (int m = 0; m < 4; ++m) _Pragma("unroll") for (int k = 0; k < 2; ++k) dst[m][k] = *(const PG8_LAS bf16x8*)(lds + PG8_SA(b, h) + aoff + m * 2048 + k * 1024); } while (0)
; #define PG8_LDB(dst, b, h) do { _Pragma("unroll") for (int n = 0; n < 2; ++n) _Pragma("unroll") for (int k = 0; k < 2; ++k) dst[n][k] = *(const PG8_LAS bf16x8*)(lds + PG8_SB(b, h) + boff + n * 2048 + k * 1024); } while (0)
; #define PG8_MMA(ai, bj, At, Bt) do { __builtin_amdgcn_s_setprio(1); _Pragma("unroll") for (int m = 0; m < 4; ++m) _Pragma("unroll") for (int n = 0; n < 2; ++n) _Pragma("unroll") for (int k = 0; k < 2; ++k) \
;         acc[ai][bj][m][n] = __builtin_amdgcn_mfma_f32_16x16x32_bf16(Bt[n][k], At[m][k], acc[ai][bj][m][n], 0, 0, 0); __builtin_amdgcn_s_setprio(0); } while (0)
; #define PG8_WAIT_V(n) asm volatile("s_waitcnt vmcnt(" #n ")" ::: "memory")
; #define PG8_WAIT_L(n) asm volatile("s_waitcnt lgkmcnt(" #n ")" ::: "memory")
; #define PG8_BAR __builtin_amdgcn_s_barrier()
; #define PG8_SCHED __builtin_amdgcn_sched_barrier(0)
; template <class Epi, class Sched, bool ALIGN_EPI = false, bool SP2 = false>
; __device__ __forceinline__ void gemm_phase(PG8_LAS unsigned char* lds, const Gemm g, const Sched& S, const Epi& E) {
;     ...
;             const bool last = (t == nt - 2);
;             const char* a1 = cA + (size_t)(t + 1) * kstep;
;             const char* a2 = last ? nA : cA + (size_t)(t + 2) * kstep; const char* b2 = last ? nB : cB + (size_t)(t + 2) * kstep;
;             const char* a3 = a2 + kstep; const char* b3 = b2 + kstep;
;             if (last && has_next) S.a_ready(nxt);
;             if constexpr (SP2) {
;             PG8_LDB(B0, 0, 0); PG8_LDB(B1, 0, 1); PG8_SCHED; PG8_LDA(At, 0, 0); PG8_STAGEA(PG8_SA(1, 1), a1, 1, false);
;             PG8_WAIT_V(8); PG8_WAIT_L(0); PG8_BAR; PG8_MMA(0, 0, At, B0); PG8_MMA(0, 1, At, B1); PG8_BAR; PG8_SCHED;
;             PG8_LDA(At, 0, 1); PG8_STAGE(PG8_SB(0, 0), b2, voffB); PG8_STAGE(PG8_SB(0, 1), b2 + hstep, voffB); PG8_STAGEA(PG8_SA(0, 0), a2, 0, last);
.LBB0_927:
	s_nop 0
	v_add_u32_e32 v147, s76, v142
	ds_read_b128 v[148:151], v147
	ds_read_b128 v[152:155], v147 offset:1024
	ds_read_b128 v[156:159], v147 offset:2048
	ds_read_b128 v[160:163], v147 offset:3072
	v_add_u32_e32 v147, s77, v142
	ds_read_b128 v[164:167], v147
	ds_read_b128 v[168:171], v147 offset:1024
	ds_read_b128 v[172:175], v147 offset:2048
	ds_read_b128 v[176:179], v147 offset:3072
	s_add_u32 s60, s58, 0xfffe0080
	s_addc_u32 s61, s59, -1
	s_cmp_eq_u32 s83, 4
	s_cselect_b32 s63, s9, s61
	s_cselect_b32 s62, s11, s60
	s_cselect_b32 s61, s36, s49
	s_cselect_b32 s60, s37, s47
	v_lshl_add_u64 v[200:201], s[58:59], 0, v[138:139]
	s_add_i32 m0, s57, 0xc000
	ds_read_b128 v[180:183], v146
	ds_read_b128 v[184:187], v146 offset:1024
	ds_read_b128 v[188:191], v146 offset:2048
	ds_read_b128 v[192:195], v146 offset:3072
	ds_read_b128 v[196:199], v146 offset:4096
	ds_read_b128 v[204:207], v146 offset:5120
	ds_read_b128 v[208:211], v146 offset:6144
	ds_read_b128 v[212:215], v146 offset:7168
	global_load_lds_dwordx4 v[200:201], off
	v_lshl_add_u64 v[200:201], s[58:59], 0, v[140:141]
	s_add_i32 m0, s57, 0xe000
	s_nop 0
	global_load_lds_dwordx4 v[200:201], off
	s_waitcnt vmcnt(8) lgkmcnt(0)
	s_barrier
	s_setprio 1
	v_mfma_f32_16x16x32_bf16 v[122:125], v[148:151], v[180:183], v[122:125]
	v_mfma_f32_16x16x32_bf16 v[126:129], v[156:159], v[180:183], v[126:129]
	v_mfma_f32_16x16x32_bf16 v[106:109], v[148:151], v[188:191], v[106:109]
	v_mfma_f32_16x16x32_bf16 v[110:113], v[156:159], v[188:191], v[110:113]
	v_mfma_f32_16x16x32_bf16 v[90:93], v[148:151], v[196:199], v[90:93]
	v_mfma_f32_16x16x32_bf16 v[94:97], v[156:159], v[196:199], v[94:97]
	v_mfma_f32_16x16x32_bf16 v[74:77], v[148:151], v[208:211], v[74:77]
	v_mfma_f32_16x16x32_bf16 v[78:81], v[156:159], v[208:211], v[78:81]
	v_mfma_f32_16x16x32_bf16 v[122:125], v[152:155], v[184:187], v[122:125]
	v_mfma_f32_16x16x32_bf16 v[126:129], v[160:163], v[184:187], v[126:129]
	v_mfma_f32_16x16x32_bf16 v[106:109], v[152:155], v[192:195], v[106:109]
	v_mfma_f32_16x16x32_bf16 v[110:113], v[160:163], v[192:195], v[110:113]
	v_mfma_f32_16x16x32_bf16 v[90:93], v[152:155], v[204:207], v[90:93]
	v_mfma_f32_16x16x32_bf16 v[94:97], v[160:163], v[204:207], v[94:97]
	v_mfma_f32_16x16x32_bf16 v[74:77], v[152:155], v[212:215], v[74:77]
	v_mfma_f32_16x16x32_bf16 v[78:81], v[160:163], v[212:215], v[78:81]
	v_mfma_f32_16x16x32_bf16 v[114:117], v[164:167], v[180:183], v[114:117]
	v_mfma_f32_16x16x32_bf16 v[118:121], v[172:175], v[180:183], v[118:121]
	v_mfma_f32_16x16x32_bf16 v[98:101], v[164:167], v[188:191], v[98:101]
	v_mfma_f32_16x16x32_bf16 v[102:105], v[172:175], v[188:191], v[102:105]
	v_mfma_f32_16x16x32_bf16 v[82:85], v[164:167], v[196:199], v[82:85]
	v_mfma_f32_16x16x32_bf16 v[86:89], v[172:175], v[196:199], v[86:89]
	v_mfma_f32_16x16x32_bf16 v[66:69], v[164:167], v[208:211], v[66:69]
	v_mfma_f32_16x16x32_bf16 v[70:73], v[172:175], v[208:211], v[70:73]
	v_mfma_f32_16x16x32_bf16 v[114:117], v[168:171], v[184:187], v[114:117]
	v_mfma_f32_16x16x32_bf16 v[118:121], v[176:179], v[184:187], v[118:121]
	v_mfma_f32_16x16x32_bf16 v[98:101], v[168:171], v[192:195], v[98:101]
	v_mfma_f32_16x16x32_bf16 v[102:105], v[176:179], v[192:195], v[102:105]
	v_mfma_f32_16x16x32_bf16 v[82:85], v[168:171], v[204:207], v[82:85]
	v_mfma_f32_16x16x32_bf16 v[86:89], v[176:179], v[204:207], v[86:89]
	v_mfma_f32_16x16x32_bf16 v[66:69], v[168:171], v[212:215], v[66:69]
	v_mfma_f32_16x16x32_bf16 v[70:73], v[176:179], v[212:215], v[70:73]
	s_setprio 0
	s_barrier
	s_nop 0
	s_add_i32 s84, s76, s65
	v_lshl_add_u64 v[200:201], s[60:61], 0, v[132:133]
	s_mov_b32 m0, s84
	ds_read_b128 v[180:183], v146 offset:16384
	ds_read_b128 v[184:187], v146 offset:17408
	ds_read_b128 v[188:191], v146 offset:18432
	ds_read_b128 v[192:195], v146 offset:19456
	ds_read_b128 v[196:199], v146 offset:20480
	ds_read_b128 v[204:207], v146 offset:21504
	ds_read_b128 v[208:211], v146 offset:22528
	ds_read_b128 v[212:215], v146 offset:23552
	global_load_lds_dwordx4 v[200:201], off
	s_add_i32 m0, s84, 0x2000
	s_add_u32 s84, s60, 0x20000
	v_lshl_add_u64 v[216:217], s[60:61], 0, v[136:137]
	s_addc_u32 s85, s61, 0
	s_add_i32 s86, s77, s65
	global_load_lds_dwordx4 v[216:217], off
	v_lshl_add_u64 v[218:219], s[84:85], 0, v[132:133]
	s_mov_b32 m0, s86
	v_lshl_add_u64 v[220:221], s[62:63], 0, v[134:135]
	global_load_lds_dwordx4 v[218:219], off
	v_lshl_add_u64 v[218:219], s[84:85], 0, v[136:137]
	s_add_i32 m0, s86, 0x2000
	s_nop 0
	global_load_lds_dwordx4 v[218:219], off
	v_lshl_add_u64 v[218:219], s[62:63], 0, v[130:131]
	s_mov_b32 m0, s57
	s_nop 0
	global_load_lds_dwordx4 v[218:219], off
	s_mov_b32 m0, s66
	s_nop 0
	global_load_lds_dwordx4 v[220:221], off
	s_waitcnt vmcnt(8) lgkmcnt(0)
	s_barrier
; #define PG8_LDA(dst, b, h) do { _Pragma("unroll") for (int m = 0; m < 4; ++m) _Pragma("unroll") for (int k = 0; k < 2; ++k) dst[m][k] = *(const PG8_LAS bf16x8*)(lds + PG8_SA(b, h) + aoff + m * 2048 + k * 1024); } while (0)
; #define PG8_LDB(dst, b, h) do { _Pragma("unroll") for (int n = 0; n < 2; ++n) _Pragma("unroll") for (int k = 0; k < 2; ++k) dst[n][k] = *(const PG8_LAS bf16x8*)(lds + PG8_SB(b, h) + boff + n * 2048 + k * 1024); } while (0)
; #define PG8_MMA(ai, bj, At, Bt) do { __builtin_amdgcn_s_setprio(1); _Pragma("unroll") for (int m = 0; m < 4; ++m) _Pragma("unroll") for (int n = 0; n < 2; ++n) _Pragma("unroll") for (int k = 0; k < 2; ++k) \
;         acc[ai][bj][m][n] = __builtin_amdgcn_mfma_f32_16x16x32_bf16(Bt[n][k], At[m][k], acc[ai][bj][m][n], 0, 0, 0); __builtin_amdgcn_s_setprio(0); } while (0)
; #define PG8_WAIT_V(n) asm volatile("s_waitcnt vmcnt(" #n ")" ::: "memory")
; #define PG8_WAIT_L(n) asm volatile("s_waitcnt lgkmcnt(" #n ")" ::: "memory")
; #define PG8_BAR __builtin_amdgcn_s_barrier()
; #define PG8_SCHED __builtin_amdgcn_sched_barrier(0)
; template <class Epi, class Sched, bool ALIGN_EPI = false, bool SP2 = false>
; __device__ __forceinline__ void gemm_phase(PG8_LAS unsigned char* lds, const Gemm g, const Sched& S, const Epi& E) {
;     ...
;             PG8_WAIT_V(8); PG8_WAIT_L(0); PG8_BAR; PG8_MMA(1, 0, At, B0); PG8_MMA(1, 1, At, B1); PG8_BAR; PG8_SCHED;
;             PG8_LDB(B0, 1, 0); PG8_LDB(B1, 1, 1); PG8_SCHED; PG8_LDA(At, 1, 0); PG8_STAGEA(PG8_SA(0, 1), a2, 1, last);
;             PG8_WAIT_V(8); PG8_WAIT_L(0); PG8_BAR; PG8_MMA(0, 0, At, B0); PG8_MMA(0, 1, At, B1); PG8_BAR; PG8_SCHED;
	s_setprio 1
	v_mfma_f32_16x16x32_bf16 v[58:61], v[148:151], v[180:183], v[58:61]
	v_mfma_f32_16x16x32_bf16 v[62:65], v[156:159], v[180:183], v[62:65]
	v_mfma_f32_16x16x32_bf16 v[42:45], v[148:151], v[188:191], v[42:45]
	v_mfma_f32_16x16x32_bf16 v[46:49], v[156:159], v[188:191], v[46:49]
	v_mfma_f32_16x16x32_bf16 v[26:29], v[148:151], v[196:199], v[26:29]
	v_mfma_f32_16x16x32_bf16 v[30:33], v[156:159], v[196:199], v[30:33]
	v_mfma_f32_16x16x32_bf16 v[10:13], v[148:151], v[208:211], v[10:13]
	v_mfma_f32_16x16x32_bf16 v[14:17], v[156:159], v[208:211], v[14:17]
	v_mfma_f32_16x16x32_bf16 v[58:61], v[152:155], v[184:187], v[58:61]
	v_mfma_f32_16x16x32_bf16 v[62:65], v[160:163], v[184:187], v[62:65]
	v_mfma_f32_16x16x32_bf16 v[42:45], v[152:155], v[192:195], v[42:45]
	v_mfma_f32_16x16x32_bf16 v[46:49], v[160:163], v[192:195], v[46:49]
	v_mfma_f32_16x16x32_bf16 v[26:29], v[152:155], v[204:207], v[26:29]
	v_mfma_f32_16x16x32_bf16 v[30:33], v[160:163], v[204:207], v[30:33]
	v_mfma_f32_16x16x32_bf16 v[10:13], v[152:155], v[212:215], v[10:13]
	v_mfma_f32_16x16x32_bf16 v[14:17], v[160:163], v[212:215], v[14:17]
	v_mfma_f32_16x16x32_bf16 v[50:53], v[164:167], v[180:183], v[50:53]
	v_mfma_f32_16x16x32_bf16 v[54:57], v[172:175], v[180:183], v[54:57]
	v_mfma_f32_16x16x32_bf16 v[34:37], v[164:167], v[188:191], v[34:37]
	v_mfma_f32_16x16x32_bf16 v[38:41], v[172:175], v[188:191], v[38:41]
	v_mfma_f32_16x16x32_bf16 v[18:21], v[164:167], v[196:199], v[18:21]
	v_mfma_f32_16x16x32_bf16 v[22:25], v[172:175], v[196:199], v[22:25]
	v_mfma_f32_16x16x32_bf16 v[6:9], v[164:167], v[208:211], v[6:9]
	v_mfma_f32_16x16x32_bf16 v[2:5], v[172:175], v[208:211], v[2:5]
	v_mfma_f32_16x16x32_bf16 v[50:53], v[168:171], v[184:187], v[50:53]
	v_mfma_f32_16x16x32_bf16 v[54:57], v[176:179], v[184:187], v[54:57]
	v_mfma_f32_16x16x32_bf16 v[34:37], v[168:171], v[192:195], v[34:37]
	v_mfma_f32_16x16x32_bf16 v[38:41], v[176:179], v[192:195], v[38:41]
	v_mfma_f32_16x16x32_bf16 v[18:21], v[168:171], v[204:207], v[18:21]
	v_mfma_f32_16x16x32_bf16 v[22:25], v[176:179], v[204:207], v[22:25]
	v_mfma_f32_16x16x32_bf16 v[6:9], v[168:171], v[212:215], v[6:9]
	v_mfma_f32_16x16x32_bf16 v[2:5], v[176:179], v[212:215], v[2:5]
	s_setprio 0
	s_barrier
	s_nop 0
	s_add_i32 s84, 0, 0x18000
	v_add_u32_e32 v147, s84, v142
	s_add_i32 s85, 0, 0x1c000
	ds_read_b128 v[148:151], v147
	ds_read_b128 v[152:155], v147 offset:1024
	ds_read_b128 v[156:159], v147 offset:2048
	ds_read_b128 v[160:163], v147 offset:3072
	v_add_u32_e32 v147, s85, v142
	ds_read_b128 v[164:167], v147
	ds_read_b128 v[168:171], v147 offset:1024
	ds_read_b128 v[172:175], v147 offset:2048
	ds_read_b128 v[176:179], v147 offset:3072
	s_add_u32 s62, s62, 0x20000
	s_addc_u32 s63, s63, 0
	s_mov_b32 m0, s67
	v_lshl_add_u64 v[222:223], s[62:63], 0, v[130:131]
	ds_read_b128 v[180:183], v146 offset:32768
	ds_read_b128 v[184:187], v146 offset:33792
	ds_read_b128 v[188:191], v146 offset:34816
	ds_read_b128 v[192:195], v146 offset:35840
	ds_read_b128 v[196:199], v146 offset:36864
	ds_read_b128 v[204:207], v146 offset:37888
	ds_read_b128 v[208:211], v146 offset:38912
	ds_read_b128 v[212:215], v146 offset:39936
	global_load_lds_dwordx4 v[222:223], off
	v_lshl_add_u64 v[222:223], s[62:63], 0, v[134:135]
	s_mov_b32 m0, s68
	s_nop 0
	global_load_lds_dwordx4 v[222:223], off
	s_waitcnt vmcnt(8) lgkmcnt(0)
	s_barrier
	s_setprio 1
	v_mfma_f32_16x16x32_bf16 v[122:125], v[148:151], v[180:183], v[122:125]
	v_mfma_f32_16x16x32_bf16 v[126:129], v[156:159], v[180:183], v[126:129]
	v_mfma_f32_16x16x32_bf16 v[106:109], v[148:151], v[188:191], v[106:109]
	v_mfma_f32_16x16x32_bf16 v[110:113], v[156:159], v[188:191], v[110:113]
	v_mfma_f32_16x16x32_bf16 v[90:93], v[148:151], v[196:199], v[90:93]
	v_mfma_f32_16x16x32_bf16 v[94:97], v[156:159], v[196:199], v[94:97]
	v_mfma_f32_16x16x32_bf16 v[74:77], v[148:151], v[208:211], v[74:77]
	v_mfma_f32_16x16x32_bf16 v[78:81], v[156:159], v[208:211], v[78:81]
	v_mfma_f32_16x16x32_bf16 v[122:125], v[152:155], v[184:187], v[122:125]
	v_mfma_f32_16x16x32_bf16 v[126:129], v[160:163], v[184:187], v[126:129]
	v_mfma_f32_16x16x32_bf16 v[106:109], v[152:155], v[192:195], v[106:109]
	v_mfma_f32_16x16x32_bf16 v[110:113], v[160:163], v[192:195], v[110:113]
	v_mfma_f32_16x16x32_bf16 v[90:93], v[152:155], v[204:207], v[90:93]
	v_mfma_f32_16x16x32_bf16 v[94:97], v[160:163], v[204:207], v[94:97]
	v_mfma_f32_16x16x32_bf16 v[74:77], v[152:155], v[212:215], v[74:77]
	v_mfma_f32_16x16x32_bf16 v[78:81], v[160:163], v[212:215], v[78:81]
	v_mfma_f32_16x16x32_bf16 v[114:117], v[164:167], v[180:183], v[114:117]
	v_mfma_f32_16x16x32_bf16 v[118:121], v[172:175], v[180:183], v[118:121]
	v_mfma_f32_16x16x32_bf16 v[98:101], v[164:167], v[188:191], v[98:101]
	v_mfma_f32_16x16x32_bf16 v[102:105], v[172:175], v[188:191], v[102:105]
	v_mfma_f32_16x16x32_bf16 v[82:85], v[164:167], v[196:199], v[82:85]
	v_mfma_f32_16x16x32_bf16 v[86:89], v[172:175], v[196:199], v[86:89]
	v_mfma_f32_16x16x32_bf16 v[66:69], v[164:167], v[208:211], v[66:69]
	v_mfma_f32_16x16x32_bf16 v[70:73], v[172:175], v[208:211], v[70:73]
	v_mfma_f32_16x16x32_bf16 v[114:117], v[168:171], v[184:187], v[114:117]
	v_mfma_f32_16x16x32_bf16 v[118:121], v[176:179], v[184:187], v[118:121]
	v_mfma_f32_16x16x32_bf16 v[98:101], v[168:171], v[192:195], v[98:101]
	v_mfma_f32_16x16x32_bf16 v[102:105], v[176:179], v[192:195], v[102:105]
	v_mfma_f32_16x16x32_bf16 v[82:85], v[168:171], v[204:207], v[82:85]
	v_mfma_f32_16x16x32_bf16 v[86:89], v[176:179], v[204:207], v[86:89]
	v_mfma_f32_16x16x32_bf16 v[66:69], v[168:171], v[212:215], v[66:69]
	v_mfma_f32_16x16x32_bf16 v[70:73], v[176:179], v[212:215], v[70:73]
	s_setprio 0
	s_barrier
; #define PG8_STAGE(bufoff, gbase, voff) do { _Pragma("unroll") for (int _i = 0; _i < 2; ++_i) \
;         __builtin_amdgcn_global_load_lds((const unsigned*)((const char*)(gbase) + (voff)[_i]), (PG8_LAS unsigned*)(lds + (bufoff) + ldsw + _i * 8192), 16, 0, 0); } while (0)
; #define PG8_LDA(dst, b, h) do { _Pragma("unroll") for (int m = 0; m < 4; ++m) _Pragma("unroll") for (int k = 0; k < 2; ++k) dst[m][k] = *(const PG8_LAS bf16x8*)(lds + PG8_SA(b, h) + aoff + m * 2048 + k * 1024); } while (0)
; #define PG8_MMA(ai, bj, At, Bt) do { __builtin_amdgcn_s_setprio(1); _Pragma("unroll") for (int m = 0; m < 4; ++m) _Pragma("unroll") for (int n = 0; n < 2; ++n) _Pragma("unroll") for (int k = 0; k < 2; ++k) \
;         acc[ai][bj][m][n] = __builtin_amdgcn_mfma_f32_16x16x32_bf16(Bt[n][k], At[m][k], acc[ai][bj][m][n], 0, 0, 0); __builtin_amdgcn_s_setprio(0); } while (0)
; #define PG8_WAIT_V(n) asm volatile("s_waitcnt vmcnt(" #n ")" ::: "memory")
; #define PG8_WAIT_L(n) asm volatile("s_waitcnt lgkmcnt(" #n ")" ::: "memory")
; #define PG8_BAR __builtin_amdgcn_s_barrier()
; #define PG8_SCHED __builtin_amdgcn_sched_barrier(0)
; template <class Epi, class Sched, bool ALIGN_EPI = false, bool SP2 = false>
; __device__ __forceinline__ void gemm_phase(PG8_LAS unsigned char* lds, const Gemm g, const Sched& S, const Epi& E) {
;     ...
;         for (; t < tend; t += 2) {
;     ...
;             PG8_LDA(At, 1, 1); PG8_STAGE(PG8_SB(1, 0), b3, voffB); PG8_STAGE(PG8_SB(1, 1), b3 + hstep, voffB); PG8_STAGEA(PG8_SA(1, 0), a3, 0, last);
;             PG8_WAIT_V(8); PG8_WAIT_L(0); PG8_BAR; PG8_MMA(1, 0, At, B0); PG8_MMA(1, 1, At, B1); PG8_BAR; PG8_SCHED;
	s_add_i32 s62, s84, s65
	v_lshl_add_u64 v[200:201], v[200:201], 0, s[18:19]
	s_mov_b32 m0, s62
	ds_read_b128 v[180:183], v146 offset:49152
	ds_read_b128 v[184:187], v146 offset:50176
	ds_read_b128 v[188:191], v146 offset:51200
	ds_read_b128 v[192:195], v146 offset:52224
	ds_read_b128 v[196:199], v146 offset:53248
	ds_read_b128 v[204:207], v146 offset:54272
	ds_read_b128 v[208:211], v146 offset:55296
	ds_read_b128 v[212:215], v146 offset:56320
	global_load_lds_dwordx4 v[200:201], off
	s_add_i32 m0, s62, 0x2000
	s_add_u32 s60, s60, 0x20080
	v_lshl_add_u64 v[200:201], v[216:217], 0, s[18:19]
	s_addc_u32 s61, s61, 0
	s_add_i32 s62, s85, s65
	global_load_lds_dwordx4 v[200:201], off
	v_lshl_add_u64 v[200:201], s[60:61], 0, v[132:133]
	s_mov_b32 m0, s62
	s_nop 0
	global_load_lds_dwordx4 v[200:201], off
	v_lshl_add_u64 v[200:201], s[60:61], 0, v[136:137]
	s_add_i32 m0, s62, 0x2000
	s_nop 0
	global_load_lds_dwordx4 v[200:201], off
	v_lshl_add_u64 v[200:201], v[218:219], 0, s[18:19]
	s_mov_b32 m0, s69
	s_nop 0
	global_load_lds_dwordx4 v[200:201], off
	v_lshl_add_u64 v[200:201], v[220:221], 0, s[18:19]
	s_mov_b32 m0, s74
	s_nop 0
	global_load_lds_dwordx4 v[200:201], off
	s_waitcnt vmcnt(8) lgkmcnt(0)
	s_barrier
	s_setprio 1
	v_mfma_f32_16x16x32_bf16 v[58:61], v[148:151], v[180:183], v[58:61]
	v_mfma_f32_16x16x32_bf16 v[62:65], v[156:159], v[180:183], v[62:65]
	v_mfma_f32_16x16x32_bf16 v[42:45], v[148:151], v[188:191], v[42:45]
	v_mfma_f32_16x16x32_bf16 v[46:49], v[156:159], v[188:191], v[46:49]
	v_mfma_f32_16x16x32_bf16 v[26:29], v[148:151], v[196:199], v[26:29]
	v_mfma_f32_16x16x32_bf16 v[30:33], v[156:159], v[196:199], v[30:33]
	v_mfma_f32_16x16x32_bf16 v[10:13], v[148:151], v[208:211], v[10:13]
	v_mfma_f32_16x16x32_bf16 v[14:17], v[156:159], v[208:211], v[14:17]
	v_mfma_f32_16x16x32_bf16 v[58:61], v[152:155], v[184:187], v[58:61]
	v_mfma_f32_16x16x32_bf16 v[62:65], v[160:163], v[184:187], v[62:65]
	v_mfma_f32_16x16x32_bf16 v[42:45], v[152:155], v[192:195], v[42:45]
	v_mfma_f32_16x16x32_bf16 v[46:49], v[160:163], v[192:195], v[46:49]
	v_mfma_f32_16x16x32_bf16 v[26:29], v[152:155], v[204:207], v[26:29]
	v_mfma_f32_16x16x32_bf16 v[30:33], v[160:163], v[204:207], v[30:33]
	v_mfma_f32_16x16x32_bf16 v[10:13], v[152:155], v[212:215], v[10:13]
	v_mfma_f32_16x16x32_bf16 v[14:17], v[160:163], v[212:215], v[14:17]
	v_mfma_f32_16x16x32_bf16 v[50:53], v[164:167], v[180:183], v[50:53]
	v_mfma_f32_16x16x32_bf16 v[54:57], v[172:175], v[180:183], v[54:57]
	v_mfma_f32_16x16x32_bf16 v[34:37], v[164:167], v[188:191], v[34:37]
	v_mfma_f32_16x16x32_bf16 v[38:41], v[172:175], v[188:191], v[38:41]
	v_mfma_f32_16x16x32_bf16 v[18:21], v[164:167], v[196:199], v[18:21]
	v_mfma_f32_16x16x32_bf16 v[22:25], v[172:175], v[196:199], v[22:25]
	v_mfma_f32_16x16x32_bf16 v[6:9], v[164:167], v[208:211], v[6:9]
	v_mfma_f32_16x16x32_bf16 v[2:5], v[172:175], v[208:211], v[2:5]
	v_mfma_f32_16x16x32_bf16 v[50:53], v[168:171], v[184:187], v[50:53]
	v_mfma_f32_16x16x32_bf16 v[54:57], v[176:179], v[184:187], v[54:57]
	v_mfma_f32_16x16x32_bf16 v[34:37], v[168:171], v[192:195], v[34:37]
	v_mfma_f32_16x16x32_bf16 v[38:41], v[176:179], v[192:195], v[38:41]
	v_mfma_f32_16x16x32_bf16 v[18:21], v[168:171], v[204:207], v[18:21]
	v_mfma_f32_16x16x32_bf16 v[22:25], v[176:179], v[204:207], v[22:25]
	v_mfma_f32_16x16x32_bf16 v[6:9], v[168:171], v[212:215], v[6:9]
	v_mfma_f32_16x16x32_bf16 v[2:5], v[176:179], v[212:215], v[2:5]
	s_setprio 0
	s_barrier
	s_add_i32 s83, s83, 2
	s_add_u32 s58, s58, 0x100
	s_addc_u32 s59, s59, 0
	s_add_u32 s47, s47, 0x100
	s_addc_u32 s49, s49, 0
	s_cmp_gt_u32 s83, 5
	s_cbranch_scc0 .LBB0_927
	s_nop 0
	s_and_b64 vcc, exec, s[24:25]
	s_cbranch_vccz .LBB0_930
	s_barrier
